# deferred weight-conversion split: all layer-1 tiles (4096 + 2048) deferred, idle-slot quotas 6/10/9/12
# baseline (speedup 1.0000x reference)
; __device__ __forceinline__ void bt_load(const float* __restrict__ src, int N, int perm, int it, int ntn, f32x4 (&v)[8]) {
;     const int wid = threadIdx.x >> 6, lane = threadIdx.x & 63;
;     const int per = 16 * ntn, z = it / per, r = it % per, kt = r / ntn, nt = r % ntn;
;     const int np = nt * 256 + lane * 4;
;     const int sc = perm ? (nt * 128 + (lane & 31) * 4 + (lane >> 5) * 1024) : np;
;     const float* p = src + (size_t)z * 1024 * N + (size_t)(kt * 64 + wid * 8) * N + sc;
; #pragma unroll
;     for (int i = 0; i < 8; ++i) v[i] = __builtin_nontemporal_load((const f32x4*)(p + (size_t)i * N));
; }
; __device__ __forceinline__ void ph_big_transpose(const float* __restrict__ src, int N, int perm, int batch, bf16* __restrict__ dst, float* tile  , int G, int ndefer) {
;     const int tid = threadIdx.x, wid = tid >> 6, lane = tid & 63, ntn = N / 256, total = batch * 16 * ntn - ndefer;
;     int it = (int)blockIdx.x;
;     if (it >= total) return;
;     f32x4 cur[8], nxt[8], nx2[8];
;     bt_load(src, N, perm, it, ntn, cur);
;     if (it + G < total) bt_load(src, N, perm, it + G, ntn, nxt);
;     for (; it < total; it += G) {
;         const bool more = it + G < total, more2 = it + 2 * G < total;
;         if (more2) bt_load(src, N, perm, it + 2 * G, ntn, nx2);
.LBB0_63:
	s_cmpk_gt_i32 s2, 0xfff
	s_waitcnt lgkmcnt(0)
	s_barrier
	s_cbranch_scc1 .LBB0_71
	s_ashr_i32 s0, s2, 31
	s_lshr_b32 s0, s0, 25
	s_add_i32 s1, s2, s0
	s_ashr_i32 s0, s1, 7
	s_and_b32 s1, s1, 0xff80
	s_sub_i32 s1, s2, s1
	s_bfe_i32 s4, s1, 0x80000
	s_bfe_u32 s4, s4, 0x3000c
	s_add_i32 s4, s1, s4
	s_bfe_i32 s5, s4, 0x80000
	s_and_b32 s4, s4, 0xf8
	v_lshlrev_b32_e32 v2, 2, v0
	s_sub_i32 s1, s1, s4
	v_and_b32_e32 v2, 0x7c, v2
	v_lshlrev_b32_e32 v3, 5, v0
	s_movk_i32 s4, 0x400
	s_sext_i32_i8 s1, s1
	v_and_or_b32 v99, v3, s4, v2
	v_lshl_add_u32 v2, s1, 7, v99
	s_ashr_i32 s1, s0, 31
	s_lshl_b64 s[0:1], s[0:1], 23
	s_sext_i32_i16 s5, s5
	s_add_u32 s0, s68, s0
	s_addc_u32 s1, s69, s1
	s_lshl_b32 s4, s5, 3
	v_lshrrev_b32_e32 v3, 3, v0
	s_andn2_b32 s4, s4, 63
	v_and_b32_e32 v110, 56, v3
	v_or_b32_e32 v4, s4, v110
	v_ashrrev_i32_e32 v5, 31, v4
	v_lshlrev_b64 v[4:5], 13, v[4:5]
	v_lshl_add_u64 v[4:5], s[0:1], 0, v[4:5]
	v_ashrrev_i32_e32 v3, 31, v2
	v_lshl_add_u64 v[2:3], v[2:3], 2, v[4:5]
	s_movk_i32 s0, 0x2000
	v_add_co_u32_e32 v4, vcc, s0, v2
	s_movk_i32 s1, 0x4000
	s_nop 0
	v_addc_co_u32_e32 v5, vcc, 0, v3, vcc
	global_load_dwordx4 v[38:41], v[2:3], off nt
	global_load_dwordx4 v[34:37], v[4:5], off nt
	v_add_co_u32_e32 v4, vcc, s1, v2
	s_movk_i32 s4, 0x6000
	s_nop 0
	v_addc_co_u32_e32 v5, vcc, 0, v3, vcc
	v_add_co_u32_e32 v6, vcc, s4, v2
	s_mov_b32 s5, 0x8000
	s_nop 0
	v_addc_co_u32_e32 v7, vcc, 0, v3, vcc
	global_load_dwordx4 v[46:49], v[4:5], off nt
	global_load_dwordx4 v[42:45], v[6:7], off nt
	v_add_co_u32_e32 v4, vcc, s5, v2
	s_mov_b32 s6, 0xa000
	s_nop 0
	v_addc_co_u32_e32 v5, vcc, 0, v3, vcc
	v_add_co_u32_e32 v6, vcc, s6, v2
	s_add_i32 s6, s62, s2
	s_nop 0
	v_addc_co_u32_e32 v7, vcc, 0, v3, vcc
	global_load_dwordx4 v[54:57], v[4:5], off nt
	global_load_dwordx4 v[50:53], v[6:7], off nt
	v_add_co_u32_e32 v4, vcc, 0xc000, v2
	s_cmpk_gt_i32 s6, 0xfff
	s_nop 0
	v_addc_co_u32_e32 v5, vcc, 0, v3, vcc
	v_add_co_u32_e32 v2, vcc, 0xe000, v2
	s_nop 1
	v_addc_co_u32_e32 v3, vcc, 0, v3, vcc
	global_load_dwordx4 v[62:65], v[4:5], off nt
	global_load_dwordx4 v[58:61], v[2:3], off nt
	s_cbranch_scc1 .LBB0_66
	s_ashr_i32 s7, s6, 31
	s_lshr_b32 s7, s7, 25
	s_add_i32 s7, s6, s7
	s_ashr_i32 s8, s7, 7
	s_and_b32 s7, s7, 0xff80
	s_sub_i32 s6, s6, s7
	s_bfe_i32 s7, s6, 0x80000
	s_bfe_u32 s7, s7, 0x3000c
	s_add_i32 s7, s6, s7
	s_bfe_i32 s9, s7, 0x80000
	s_and_b32 s7, s7, 0xf8
	s_sub_i32 s6, s6, s7
	s_sext_i32_i16 s10, s9
	s_sext_i32_i8 s6, s6
	s_ashr_i32 s9, s8, 31
	v_lshl_add_u32 v2, s6, 7, v99
	s_lshl_b64 s[6:7], s[8:9], 23
	s_add_u32 s6, s68, s6
	s_addc_u32 s7, s69, s7
	s_lshl_b32 s8, s10, 3
	s_andn2_b32 s8, s8, 63
	v_or_b32_e32 v4, s8, v110
	v_ashrrev_i32_e32 v5, 31, v4
	v_lshlrev_b64 v[4:5], 13, v[4:5]
	v_lshl_add_u64 v[4:5], s[6:7], 0, v[4:5]
	v_ashrrev_i32_e32 v3, 31, v2
	v_lshl_add_u64 v[26:27], v[2:3], 2, v[4:5]
	v_add_co_u32_e32 v6, vcc, s0, v26
	s_nop 1
	v_addc_co_u32_e32 v7, vcc, 0, v27, vcc
	v_add_co_u32_e32 v10, vcc, s1, v26
	global_load_dwordx4 v[2:5], v[26:27], off nt
	s_nop 0
	global_load_dwordx4 v[6:9], v[6:7], off nt
	v_addc_co_u32_e32 v11, vcc, 0, v27, vcc
	v_add_co_u32_e32 v14, vcc, s4, v26
	s_nop 1
	v_addc_co_u32_e32 v15, vcc, 0, v27, vcc
	v_add_co_u32_e32 v18, vcc, s5, v26
	global_load_dwordx4 v[10:13], v[10:11], off nt
	s_nop 0
	global_load_dwordx4 v[14:17], v[14:15], off nt
	v_addc_co_u32_e32 v19, vcc, 0, v27, vcc
	v_add_co_u32_e32 v22, vcc, 0xa000, v26
	s_nop 1
	v_addc_co_u32_e32 v23, vcc, 0, v27, vcc
	v_add_co_u32_e32 v28, vcc, 0xc000, v26
	global_load_dwordx4 v[18:21], v[18:19], off nt
	s_nop 0
	global_load_dwordx4 v[22:25], v[22:23], off nt
	v_addc_co_u32_e32 v29, vcc, 0, v27, vcc
	v_add_co_u32_e32 v30, vcc, 0xe000, v26
	s_nop 1
	v_addc_co_u32_e32 v31, vcc, 0, v27, vcc
	global_load_dwordx4 v[26:29], v[28:29], off nt
	s_nop 0
	global_load_dwordx4 v[30:33], v[30:31], off nt

; __device__ __forceinline__ unsigned g8_cvt_pk(float lo, float hi) { unsigned r; asm volatile("v_cvt_pk_bf16_f32 %0, %1, %2" : "=v"(r) : "v"(lo), "v"(hi)); return r; }
; __device__ __forceinline__ void ph_big_transpose(const float* __restrict__ src, int N, int perm, int batch, bf16* __restrict__ dst, float* tile  , int G, int ndefer) {
;     ...
;     for (; it < total; it += G) {
;         const bool more = it + G < total, more2 = it + 2 * G < total;
;         if (more2) bt_load(src, N, perm, it + 2 * G, ntn, nx2);
;         __syncthreads();
; #pragma unroll
;         for (int i = 0; i < 8; ++i) { float* t = tile + (wid * 8 + i) * 257 + lane * 4; t[0] = cur[i][0]; t[1] = cur[i][1]; t[2] = cur[i][2]; t[3] = cur[i][3]; }
;         __syncthreads();
;         const int per = 16 * ntn, z = it / per, r = it % per, kt = r / ntn, nt = r % ntn;
;         bf16* d = dst + (size_t)z * N * 1024 + (((size_t)nt * 16 + kt) << 14);
;         const int kc = lane & 7;
; #pragma unroll
;         for (int pss = 0; pss < 4; ++pss) {
;             const int n = wid * 32 + pss * 8 + (lane >> 3); float f[8];
; #pragma unroll
;             for (int j = 0; j < 8; ++j) f[j] = tile[(kc * 8 + j) * 257 + n];
;             u32x4 w; w.x = g8_cvt_pk(f[0], f[1]); w.y = g8_cvt_pk(f[2], f[3]); w.z = g8_cvt_pk(f[4], f[5]); w.w = g8_cvt_pk(f[6], f[7]);
;             __builtin_nontemporal_store(w, (u32x4*)(d + n * 64 + kc * 8));
;         }
;         if (more) {
; #pragma unroll
;             for (int i = 0; i < 8; ++i) { cur[i] = nxt[i]; nxt[i] = nx2[i]; } }
;     }
.LBB0_67:
	s_barrier
	s_waitcnt vmcnt(7)
	ds_write_b128 v111, v[38:41]
	v_add_u32_e32 v38, 0x404, v111
	s_ashr_i32 s9, s8, 31
	s_waitcnt vmcnt(6)
	ds_write2_b32 v38, v34, v35 offset1:1
	v_add_u32_e32 v34, 0x40c, v111
	s_lshr_b32 s9, s9, 25
	ds_write2_b32 v34, v36, v37 offset1:1
	v_add_u32_e32 v34, 0x808, v111
	s_add_i32 s9, s8, s9
	s_waitcnt vmcnt(5)
	ds_write2_b64 v34, v[46:47], v[48:49] offset1:1
	v_add_u32_e32 v34, 0xc0c, v111
	s_ashr_i32 s10, s9, 7
	s_and_b32 s9, s9, 0xff80
	s_waitcnt vmcnt(4)
	ds_write2_b32 v34, v42, v43 offset1:1
	v_add_u32_e32 v34, 0xc14, v111
	s_sub_i32 s9, s8, s9
	s_add_i32 s31, s8, s62
	ds_write2_b32 v34, v44, v45 offset1:1
	s_waitcnt vmcnt(3)
	ds_write_b128 v111, v[54:57] offset:4112
	v_add_u32_e32 v34, 0x1414, v111
	s_bfe_i32 s8, s9, 0x80000
	s_waitcnt vmcnt(2)
	ds_write2_b32 v34, v50, v51 offset1:1
	v_add_u32_e32 v34, 0x141c, v111
	s_bfe_u32 s8, s8, 0x3000c
	ds_write2_b32 v34, v52, v53 offset1:1
	v_add_u32_e32 v34, 0x1818, v111
	s_add_i32 s11, s9, s8
	s_waitcnt vmcnt(1)
	ds_write2_b64 v34, v[62:63], v[64:65] offset1:1
	v_add_u32_e32 v34, 0x1c1c, v111
	s_bfe_i32 s8, s11, 0x80000
	s_and_b32 s11, s11, 0xf8
	s_waitcnt vmcnt(0)
	ds_write2_b32 v34, v58, v59 offset1:1
	v_add_u32_e32 v34, 0x1c24, v111
	s_sext_i32_i16 s8, s8
	s_sub_i32 s30, s9, s11
	s_ashr_i32 s11, s10, 31
	ds_write2_b32 v34, v60, v61 offset1:1
	s_waitcnt lgkmcnt(0)
	s_barrier
	s_lshr_b32 s8, s8, 3
	s_lshl_b64 s[10:11], s[10:11], 22
	ds_read_b32 v34, v112 offset:1028
	ds_read_b32 v35, v112 offset:3084
	ds_read_b32 v36, v112 offset:5140
	ds_read_b32 v37, v112 offset:7196
	ds_read_b32 v38, v112 offset:6168
	ds_read_b32 v39, v112 offset:4112
	ds_read_b32 v40, v112 offset:2056
	ds_read_b32 v41, v112
	s_add_u32 s33, s5, s10
	s_addc_u32 s34, s6, s11
	s_bfe_i64 s[10:11], s[30:31], 0x80000
	s_bfe_i64 s[8:9], s[8:9], 0x100000
	s_lshl_b64 s[10:11], s[10:11], 19
	s_add_u32 s10, s33, s10
	s_addc_u32 s11, s34, s11
	s_lshl_b64 s[8:9], s[8:9], 15
	s_waitcnt lgkmcnt(0)
	v_cvt_pk_bf16_f32 v34, v41, v34
	v_cvt_pk_bf16_f32 v35, v40, v35
	v_cvt_pk_bf16_f32 v36, v39, v36
	v_cvt_pk_bf16_f32 v37, v38, v37
	ds_read_b32 v42, v112 offset:1060
	ds_read_b32 v43, v112 offset:3116
	ds_read_b32 v44, v112 offset:5172
	ds_read_b32 v45, v112 offset:7228
	ds_read_b32 v46, v112 offset:6200
	ds_read_b32 v47, v112 offset:4144
	ds_read_b32 v48, v112 offset:2088
	ds_read_b32 v49, v112 offset:32
	s_add_u32 s8, s10, s8
	s_addc_u32 s9, s11, s9
	v_lshl_add_u64 v[38:39], s[8:9], 0, v[100:101]
	v_mov_b32_e32 v103, v101
	v_lshl_add_u64 v[40:41], v[38:39], 0, v[102:103]
	global_store_dwordx4 v[40:41], v[34:37], off nt
	v_mov_b32_e32 v105, v101
	v_lshl_add_u64 v[40:41], v[38:39], 0, v[104:105]
	s_waitcnt lgkmcnt(0)
	v_cvt_pk_bf16_f32 v34, v49, v42
	v_cvt_pk_bf16_f32 v35, v48, v43
	v_cvt_pk_bf16_f32 v36, v47, v44
	v_cvt_pk_bf16_f32 v37, v46, v45
	ds_read_b32 v42, v112 offset:1092
	ds_read_b32 v43, v112 offset:3148
	ds_read_b32 v44, v112 offset:5204
	ds_read_b32 v45, v112 offset:6232
	ds_read_b32 v46, v112 offset:4176
	ds_read_b32 v47, v112 offset:2120
	ds_read_b32 v48, v112 offset:64
	ds_read_b32 v49, v112 offset:7260
	global_store_dwordx4 v[40:41], v[34:37], off nt
	v_mov_b32_e32 v107, v101
	v_lshl_add_u64 v[40:41], v[38:39], 0, v[106:107]
	s_waitcnt lgkmcnt(1)
	v_cvt_pk_bf16_f32 v34, v48, v42
	v_cvt_pk_bf16_f32 v35, v47, v43
	v_cvt_pk_bf16_f32 v36, v46, v44
	s_waitcnt lgkmcnt(0)
	v_cvt_pk_bf16_f32 v37, v45, v49
	ds_read_b32 v42, v112 offset:1124
	ds_read_b32 v43, v112 offset:3180
	ds_read_b32 v44, v112 offset:5236
	ds_read_b32 v45, v112 offset:6264
	ds_read_b32 v46, v112 offset:4208
	ds_read_b32 v47, v112 offset:2152
	ds_read_b32 v48, v112 offset:96
	ds_read_b32 v49, v112 offset:7292
	v_mov_b32_e32 v109, v101
	global_store_dwordx4 v[40:41], v[34:37], off nt
	v_lshl_add_u64 v[38:39], v[38:39], 0, v[108:109]
	v_mov_b64_e32 v[60:61], v[32:33]
	s_waitcnt lgkmcnt(1)
	v_cvt_pk_bf16_f32 v34, v48, v42
	v_cvt_pk_bf16_f32 v35, v47, v43
	v_cvt_pk_bf16_f32 v36, v46, v44
	s_waitcnt lgkmcnt(0)
	v_cvt_pk_bf16_f32 v37, v45, v49
	global_store_dwordx4 v[38:39], v[34:37], off nt
	v_mov_b64_e32 v[64:65], v[28:29]
	v_mov_b64_e32 v[52:53], v[24:25]
	v_mov_b64_e32 v[56:57], v[20:21]
	v_mov_b64_e32 v[44:45], v[16:17]
	v_mov_b64_e32 v[48:49], v[12:13]
	v_mov_b64_e32 v[36:37], v[8:9]
	v_mov_b64_e32 v[40:41], v[4:5]
	v_mov_b64_e32 v[58:59], v[30:31]
	v_mov_b64_e32 v[62:63], v[26:27]
	v_mov_b64_e32 v[50:51], v[22:23]
	v_mov_b64_e32 v[54:55], v[18:19]
	v_mov_b64_e32 v[42:43], v[14:15]
	v_mov_b64_e32 v[46:47], v[10:11]
	v_mov_b64_e32 v[34:35], v[6:7]
	v_mov_b64_e32 v[38:39], v[2:3]
	v_mov_b64_e32 v[30:31], v[94:95]
	v_mov_b64_e32 v[26:27], v[90:91]
	v_mov_b64_e32 v[22:23], v[86:87]
	v_mov_b64_e32 v[18:19], v[82:83]
	v_mov_b64_e32 v[14:15], v[78:79]
	v_mov_b64_e32 v[10:11], v[74:75]
	v_mov_b64_e32 v[6:7], v[70:71]
	v_mov_b64_e32 v[2:3], v[66:67]
	s_cmpk_lt_i32 s31, 0x1000
	v_mov_b64_e32 v[32:33], v[96:97]
	v_mov_b64_e32 v[28:29], v[92:93]
	v_mov_b64_e32 v[24:25], v[88:89]
	v_mov_b64_e32 v[20:21], v[84:85]
	v_mov_b64_e32 v[16:17], v[80:81]
	v_mov_b64_e32 v[12:13], v[76:77]
	v_mov_b64_e32 v[8:9], v[72:73]
	v_mov_b64_e32 v[4:5], v[68:69]
	s_mov_b32 s8, s31
	s_cbranch_scc0 .LBB0_70
; __device__ __forceinline__ void bt_load(const float* __restrict__ src, int N, int perm, int it, int ntn, f32x4 (&v)[8]) {
;     const int wid = threadIdx.x >> 6, lane = threadIdx.x & 63;
;     const int per = 16 * ntn, z = it / per, r = it % per, kt = r / ntn, nt = r % ntn;
;     const int np = nt * 256 + lane * 4;
;     const int sc = perm ? (nt * 128 + (lane & 31) * 4 + (lane >> 5) * 1024) : np;
;     const float* p = src + (size_t)z * 1024 * N + (size_t)(kt * 64 + wid * 8) * N + sc;
; #pragma unroll
;     for (int i = 0; i < 8; ++i) v[i] = __builtin_nontemporal_load((const f32x4*)(p + (size_t)i * N));
; }
; __device__ __forceinline__ void ph_big_transpose(const float* __restrict__ src, int N, int perm, int batch, bf16* __restrict__ dst, float* tile  , int G, int ndefer) {
;     ...
;         const bool more = it + G < total, more2 = it + 2 * G < total;
;         if (more2) bt_load(src, N, perm, it + 2 * G, ntn, nx2);
.LBB0_68:
	s_add_i32 s9, s7, s8
	s_cmpk_gt_i32 s9, 0xfff
	s_cbranch_scc1 .LBB0_67
	s_ashr_i32 s10, s9, 31
	s_lshr_b32 s10, s10, 25
	s_add_i32 s11, s9, s10
	s_ashr_i32 s10, s11, 7
	s_and_b32 s11, s11, 0xff80
	s_sub_i32 s9, s9, s11
	s_bfe_i32 s11, s9, 0x80000
	s_bfe_u32 s11, s11, 0x3000c
	s_add_i32 s11, s9, s11
	s_bfe_i32 s30, s11, 0x80000
	s_and_b32 s11, s11, 0xf8
	s_sub_i32 s9, s9, s11
	s_ashr_i32 s11, s10, 31
	s_lshl_b64 s[10:11], s[10:11], 23
	s_sext_i32_i16 s30, s30
	s_sext_i32_i8 s9, s9
	s_add_u32 s10, s68, s10
	v_lshl_add_u32 v66, s9, 7, v99
	s_addc_u32 s11, s69, s11
	s_lshl_b32 s9, s30, 3
	s_andn2_b32 s9, s9, 63
	v_or_b32_e32 v68, s9, v110
	v_ashrrev_i32_e32 v69, 31, v68
	v_lshlrev_b64 v[68:69], 13, v[68:69]
	v_lshl_add_u64 v[68:69], s[10:11], 0, v[68:69]
	v_ashrrev_i32_e32 v67, 31, v66
	v_lshl_add_u64 v[90:91], v[66:67], 2, v[68:69]
	v_add_co_u32_e32 v70, vcc, s0, v90
	s_nop 1
	v_addc_co_u32_e32 v71, vcc, 0, v91, vcc
	v_add_co_u32_e32 v74, vcc, s1, v90
	global_load_dwordx4 v[66:69], v[90:91], off nt
	s_nop 0
	global_load_dwordx4 v[70:73], v[70:71], off nt
	v_addc_co_u32_e32 v75, vcc, 0, v91, vcc
	v_add_co_u32_e32 v78, vcc, s4, v90
	s_nop 1
	v_addc_co_u32_e32 v79, vcc, 0, v91, vcc
	v_add_co_u32_e32 v82, vcc, 0x8000, v90
	global_load_dwordx4 v[74:77], v[74:75], off nt
	s_nop 0
	global_load_dwordx4 v[78:81], v[78:79], off nt
	v_addc_co_u32_e32 v83, vcc, 0, v91, vcc
	v_add_co_u32_e32 v86, vcc, 0xa000, v90
	s_nop 1
	v_addc_co_u32_e32 v87, vcc, 0, v91, vcc
	v_add_co_u32_e32 v92, vcc, 0xc000, v90
	global_load_dwordx4 v[82:85], v[82:83], off nt
	s_nop 0
	global_load_dwordx4 v[86:89], v[86:87], off nt
	v_addc_co_u32_e32 v93, vcc, 0, v91, vcc
	v_add_co_u32_e32 v94, vcc, 0xe000, v90
	s_nop 1
	v_addc_co_u32_e32 v95, vcc, 0, v91, vcc
	global_load_dwordx4 v[90:93], v[92:93], off nt
	s_nop 0
	global_load_dwordx4 v[94:97], v[94:95], off nt
	s_branch .LBB0_67

; __device__ __forceinline__ void bt_load(const float* __restrict__ src, int N, int perm, int it, int ntn, f32x4 (&v)[8]) {
;     const int wid = threadIdx.x >> 6, lane = threadIdx.x & 63;
;     const int per = 16 * ntn, z = it / per, r = it % per, kt = r / ntn, nt = r % ntn;
;     const int np = nt * 256 + lane * 4;
;     const int sc = perm ? (nt * 128 + (lane & 31) * 4 + (lane >> 5) * 1024) : np;
;     const float* p = src + (size_t)z * 1024 * N + (size_t)(kt * 64 + wid * 8) * N + sc;
; #pragma unroll
;     for (int i = 0; i < 8; ++i) v[i] = __builtin_nontemporal_load((const f32x4*)(p + (size_t)i * N));
; }
; __device__ __forceinline__ void ph_big_transpose(const float* __restrict__ src, int N, int perm, int batch, bf16* __restrict__ dst, float* tile  , int G, int ndefer) {
;     const int tid = threadIdx.x, wid = tid >> 6, lane = tid & 63, ntn = N / 256, total = batch * 16 * ntn - ndefer;
;     int it = (int)blockIdx.x;
;     if (it >= total) return;
;     f32x4 cur[8], nxt[8], nx2[8];
;     bt_load(src, N, perm, it, ntn, cur);
;     if (it + G < total) bt_load(src, N, perm, it + G, ntn, nxt);
.LBB0_71:
	s_cmpk_gt_i32 s2, 0x7ff
	s_cbranch_scc1 .LBB0_79
	s_ashr_i32 s0, s2, 31
	s_lshr_b32 s0, s0, 26
	s_add_i32 s1, s2, s0
	s_ashr_i32 s0, s1, 6
	s_and_b32 s1, s1, 0xffc0
	s_sub_i32 s1, s2, s1
	s_bfe_i32 s4, s1, 0x80000
	s_bfe_u32 s4, s4, 0x2000d
	s_add_i32 s4, s1, s4
	s_bfe_i32 s5, s4, 0x80000
	s_and_b32 s4, s4, 0xfc
	s_sub_i32 s1, s1, s4
	v_lshlrev_b32_e32 v2, 2, v0
	s_sext_i32_i8 s1, s1
	v_and_b32_e32 v99, 0xfc, v2
	v_lshl_or_b32 v2, s1, 8, v99
	s_ashr_i32 s1, s0, 31
	s_lshl_b64 s[0:1], s[0:1], 22
	s_sext_i32_i16 s5, s5
	s_add_u32 s0, s72, s0
	s_addc_u32 s1, s73, s1
	s_lshl_b32 s4, s5, 4
	v_lshrrev_b32_e32 v3, 3, v0
	s_andn2_b32 s4, s4, 63
	v_and_b32_e32 v110, 56, v3
	v_or_b32_e32 v4, s4, v110
	v_ashrrev_i32_e32 v5, 31, v4
	v_lshlrev_b64 v[4:5], 12, v[4:5]
	v_lshl_add_u64 v[4:5], s[0:1], 0, v[4:5]
	v_ashrrev_i32_e32 v3, 31, v2
	v_lshl_add_u64 v[2:3], v[2:3], 2, v[4:5]
	s_movk_i32 s0, 0x2000
	v_add_co_u32_e32 v4, vcc, s0, v2
	s_movk_i32 s4, 0x4000
	s_nop 0
	v_addc_co_u32_e32 v5, vcc, 0, v3, vcc
	global_load_dwordx4 v[42:45], v[4:5], off offset:-4096 nt
	global_load_dwordx4 v[34:37], v[4:5], off nt
	v_add_co_u32_e32 v4, vcc, s4, v2
	s_movk_i32 s1, 0x5000
	s_nop 0
	v_addc_co_u32_e32 v5, vcc, 0, v3, vcc
	global_load_dwordx4 v[46:49], v[4:5], off offset:-4096 nt
	global_load_dwordx4 v[38:41], v[4:5], off nt
	v_add_co_u32_e32 v4, vcc, s1, v2
	s_add_i32 s5, s62, s2
	s_nop 0
	v_addc_co_u32_e32 v5, vcc, 0, v3, vcc
	global_load_dwordx4 v[62:65], v[2:3], off nt
	global_load_dwordx4 v[50:53], v[4:5], off nt
	v_add_co_u32_e32 v4, vcc, 0x6000, v2
	s_cmpk_gt_i32 s5, 0x7ff
	s_nop 0
	v_addc_co_u32_e32 v5, vcc, 0, v3, vcc
	v_add_co_u32_e32 v2, vcc, 0x7000, v2
	s_movk_i32 s1, 0x3000
	s_nop 0
	v_addc_co_u32_e32 v3, vcc, 0, v3, vcc
	global_load_dwordx4 v[58:61], v[4:5], off nt
	global_load_dwordx4 v[54:57], v[2:3], off nt
	s_cbranch_scc1 .LBB0_74
	s_ashr_i32 s6, s5, 31
	s_lshr_b32 s6, s6, 26
	s_add_i32 s7, s5, s6
	s_ashr_i32 s6, s7, 6
	s_and_b32 s7, s7, 0xffc0
	s_sub_i32 s5, s5, s7
	s_bfe_i32 s7, s5, 0x80000
	s_bfe_u32 s7, s7, 0x2000d
	s_add_i32 s7, s5, s7
	s_bfe_i32 s8, s7, 0x80000
	s_and_b32 s7, s7, 0xfc
	s_sub_i32 s5, s5, s7
	s_ashr_i32 s7, s6, 31
	s_lshl_b64 s[6:7], s[6:7], 22
	s_sext_i32_i16 s8, s8
	s_sext_i32_i8 s5, s5
	s_add_u32 s6, s72, s6
	v_lshl_or_b32 v2, s5, 8, v99
	s_addc_u32 s7, s73, s7
	s_lshl_b32 s5, s8, 4
	s_andn2_b32 s5, s5, 63
	v_or_b32_e32 v4, s5, v110
	v_ashrrev_i32_e32 v5, 31, v4
	v_lshlrev_b64 v[4:5], 12, v[4:5]
	v_lshl_add_u64 v[4:5], s[6:7], 0, v[4:5]
	v_ashrrev_i32_e32 v3, 31, v2
	v_lshl_add_u64 v[26:27], v[2:3], 2, v[4:5]
	v_add_co_u32_e32 v2, vcc, s0, v26
	s_nop 1
	v_addc_co_u32_e32 v3, vcc, 0, v27, vcc
	v_add_co_u32_e32 v10, vcc, s4, v26
	global_load_dwordx4 v[6:9], v[2:3], off offset:-4096 nt
	s_nop 0
	global_load_dwordx4 v[2:5], v[2:3], off nt
	v_addc_co_u32_e32 v11, vcc, 0, v27, vcc
	v_add_co_u32_e32 v18, vcc, 0x5000, v26
	global_load_dwordx4 v[14:17], v[10:11], off offset:-4096 nt
	s_nop 0
	global_load_dwordx4 v[10:13], v[10:11], off nt
	v_addc_co_u32_e32 v19, vcc, 0, v27, vcc
	v_add_co_u32_e32 v28, vcc, 0x6000, v26
	global_load_dwordx4 v[22:25], v[26:27], off nt
	s_nop 0
	global_load_dwordx4 v[18:21], v[18:19], off nt
	v_addc_co_u32_e32 v29, vcc, 0, v27, vcc
	v_add_co_u32_e32 v30, vcc, 0x7000, v26
	s_nop 1
	v_addc_co_u32_e32 v31, vcc, 0, v27, vcc
	global_load_dwordx4 v[26:29], v[28:29], off nt
	s_nop 0
	global_load_dwordx4 v[30:33], v[30:31], off nt

; __device__ __forceinline__ unsigned g8_cvt_pk(float lo, float hi) { unsigned r; asm volatile("v_cvt_pk_bf16_f32 %0, %1, %2" : "=v"(r) : "v"(lo), "v"(hi)); return r; }
; __device__ __forceinline__ void bt_load(const float* __restrict__ src, int N, int perm, int it, int ntn, f32x4 (&v)[8]) {
;     const int wid = threadIdx.x >> 6, lane = threadIdx.x & 63;
;     const int per = 16 * ntn, z = it / per, r = it % per, kt = r / ntn, nt = r % ntn;
;     const int np = nt * 256 + lane * 4;
;     const int sc = perm ? (nt * 128 + (lane & 31) * 4 + (lane >> 5) * 1024) : np;
;     const float* p = src + (size_t)z * 1024 * N + (size_t)(kt * 64 + wid * 8) * N + sc;
; #pragma unroll
;     for (int i = 0; i < 8; ++i) v[i] = __builtin_nontemporal_load((const f32x4*)(p + (size_t)i * N));
; }
; __device__ __forceinline__ void ph_big_transpose(const float* __restrict__ src, int N, int perm, int batch, bf16* __restrict__ dst, float* tile  , int G, int ndefer) {
;     ...
;     for (; it < total; it += G) {
;         const bool more = it + G < total, more2 = it + 2 * G < total;
;         if (more2) bt_load(src, N, perm, it + 2 * G, ntn, nx2);
;         __syncthreads();
; #pragma unroll
;         for (int i = 0; i < 8; ++i) { float* t = tile + (wid * 8 + i) * 257 + lane * 4; t[0] = cur[i][0]; t[1] = cur[i][1]; t[2] = cur[i][2]; t[3] = cur[i][3]; }
;         __syncthreads();
;         const int per = 16 * ntn, z = it / per, r = it % per, kt = r / ntn, nt = r % ntn;
;         bf16* d = dst + (size_t)z * N * 1024 + (((size_t)nt * 16 + kt) << 14);
;         const int kc = lane & 7;
; #pragma unroll
;         for (int pss = 0; pss < 4; ++pss) {
;             const int n = wid * 32 + pss * 8 + (lane >> 3); float f[8];
; #pragma unroll
;             for (int j = 0; j < 8; ++j) f[j] = tile[(kc * 8 + j) * 257 + n];
;             u32x4 w; w.x = g8_cvt_pk(f[0], f[1]); w.y = g8_cvt_pk(f[2], f[3]); w.z = g8_cvt_pk(f[4], f[5]); w.w = g8_cvt_pk(f[6], f[7]);
;             __builtin_nontemporal_store(w, (u32x4*)(d + n * 64 + kc * 8));
;         }
;         if (more) {
; #pragma unroll
;             for (int i = 0; i < 8; ++i) { cur[i] = nxt[i]; nxt[i] = nx2[i]; } }
;     }
.LBB0_75:
	s_ashr_i32 s8, s3, 31
	s_barrier
	s_waitcnt vmcnt(3)
	ds_write_b128 v111, v[62:65]
	v_add_u32_e32 v62, 0x404, v111
	s_lshr_b32 s8, s8, 26
	ds_write2_b32 v62, v42, v43 offset1:1
	v_add_u32_e32 v42, 0x40c, v111
	s_add_i32 s9, s3, s8
	ds_write2_b32 v42, v44, v45 offset1:1
	v_add_u32_e32 v42, 0x808, v111
	s_ashr_i32 s8, s9, 6
	s_and_b32 s9, s9, 0xffc0
	s_add_i32 s7, s3, s62
	ds_write2_b64 v42, v[34:35], v[36:37] offset1:1
	v_add_u32_e32 v34, 0xc0c, v111
	s_sub_i32 s3, s3, s9
	ds_write2_b32 v34, v46, v47 offset1:1
	v_add_u32_e32 v34, 0xc14, v111
	s_bfe_i32 s9, s3, 0x80000
	ds_write2_b32 v34, v48, v49 offset1:1
	ds_write_b128 v111, v[38:41] offset:4112
	v_add_u32_e32 v34, 0x1414, v111
	s_bfe_u32 s9, s9, 0x2000d
	s_waitcnt vmcnt(2)
	ds_write2_b32 v34, v50, v51 offset1:1
	v_add_u32_e32 v34, 0x141c, v111
	s_add_i32 s9, s3, s9
	ds_write2_b32 v34, v52, v53 offset1:1
	v_add_u32_e32 v34, 0x1818, v111
	s_bfe_i32 s10, s9, 0x80000
	s_and_b32 s9, s9, 0xfc
	s_waitcnt vmcnt(1)
	ds_write2_b64 v34, v[58:59], v[60:61] offset1:1
	v_add_u32_e32 v34, 0x1c1c, v111
	s_sext_i32_i16 s10, s10
	s_sub_i32 s30, s3, s9
	s_ashr_i32 s9, s8, 31
	s_waitcnt vmcnt(0)
	ds_write2_b32 v34, v54, v55 offset1:1
	v_add_u32_e32 v34, 0x1c24, v111
	s_lshr_b32 s10, s10, 2
	s_lshl_b64 s[8:9], s[8:9], 21
	ds_write2_b32 v34, v56, v57 offset1:1
	s_waitcnt lgkmcnt(0)
	s_barrier
	s_add_u32 s3, s4, s8
	ds_read_b32 v34, v112 offset:1028
	ds_read_b32 v35, v112 offset:3084
	ds_read_b32 v36, v112 offset:5140
	ds_read_b32 v37, v112 offset:7196
	ds_read_b32 v38, v112 offset:6168
	ds_read_b32 v39, v112 offset:4112
	ds_read_b32 v40, v112 offset:2056
	ds_read_b32 v41, v112
	s_addc_u32 s31, s5, s9
	s_bfe_i64 s[8:9], s[30:31], 0x80000
	s_bfe_i64 s[10:11], s[10:11], 0x100000
	s_lshl_b64 s[8:9], s[8:9], 19
	s_add_u32 s3, s3, s8
	s_addc_u32 s30, s31, s9
	s_lshl_b64 s[8:9], s[10:11], 15
	s_waitcnt lgkmcnt(0)
	v_cvt_pk_bf16_f32 v34, v41, v34
	v_cvt_pk_bf16_f32 v35, v40, v35
	v_cvt_pk_bf16_f32 v36, v39, v36
	v_cvt_pk_bf16_f32 v37, v38, v37
	ds_read_b32 v42, v112 offset:1060
	ds_read_b32 v43, v112 offset:3116
	ds_read_b32 v44, v112 offset:5172
	ds_read_b32 v45, v112 offset:7228
	ds_read_b32 v46, v112 offset:6200
	ds_read_b32 v47, v112 offset:4144
	ds_read_b32 v48, v112 offset:2088
	ds_read_b32 v49, v112 offset:32
	s_add_u32 s8, s3, s8
	s_addc_u32 s9, s30, s9
	v_lshl_add_u64 v[38:39], s[8:9], 0, v[100:101]
	v_mov_b32_e32 v103, v101
	v_lshl_add_u64 v[40:41], v[38:39], 0, v[102:103]
	global_store_dwordx4 v[40:41], v[34:37], off nt
	v_mov_b32_e32 v105, v101
	v_lshl_add_u64 v[40:41], v[38:39], 0, v[104:105]
	s_waitcnt lgkmcnt(0)
	v_cvt_pk_bf16_f32 v34, v49, v42
	v_cvt_pk_bf16_f32 v35, v48, v43
	v_cvt_pk_bf16_f32 v36, v47, v44
	v_cvt_pk_bf16_f32 v37, v46, v45
	ds_read_b32 v42, v112 offset:1092
	ds_read_b32 v43, v112 offset:3148
	ds_read_b32 v44, v112 offset:5204
	ds_read_b32 v45, v112 offset:6232
	ds_read_b32 v46, v112 offset:4176
	ds_read_b32 v47, v112 offset:2120
	ds_read_b32 v48, v112 offset:64
	ds_read_b32 v49, v112 offset:7260
	global_store_dwordx4 v[40:41], v[34:37], off nt
	v_mov_b32_e32 v107, v101
	v_lshl_add_u64 v[40:41], v[38:39], 0, v[106:107]
	s_waitcnt lgkmcnt(1)
	v_cvt_pk_bf16_f32 v34, v48, v42
	v_cvt_pk_bf16_f32 v35, v47, v43
	v_cvt_pk_bf16_f32 v36, v46, v44
	s_waitcnt lgkmcnt(0)
	v_cvt_pk_bf16_f32 v37, v45, v49
	ds_read_b32 v42, v112 offset:1124
	ds_read_b32 v43, v112 offset:3180
	ds_read_b32 v44, v112 offset:5236
	ds_read_b32 v45, v112 offset:6264
	ds_read_b32 v46, v112 offset:4208
	ds_read_b32 v47, v112 offset:2152
	ds_read_b32 v48, v112 offset:96
	ds_read_b32 v49, v112 offset:7292
	v_mov_b32_e32 v109, v101
	global_store_dwordx4 v[40:41], v[34:37], off nt
	v_lshl_add_u64 v[38:39], v[38:39], 0, v[108:109]
	v_mov_b64_e32 v[56:57], v[32:33]
	s_waitcnt lgkmcnt(1)
	v_cvt_pk_bf16_f32 v34, v48, v42
	v_cvt_pk_bf16_f32 v35, v47, v43
	v_cvt_pk_bf16_f32 v36, v46, v44
	s_waitcnt lgkmcnt(0)
	v_cvt_pk_bf16_f32 v37, v45, v49
	global_store_dwordx4 v[38:39], v[34:37], off nt
	v_mov_b64_e32 v[60:61], v[28:29]
	v_mov_b64_e32 v[52:53], v[20:21]
	v_mov_b64_e32 v[40:41], v[12:13]
	v_mov_b64_e32 v[48:49], v[16:17]
	v_mov_b64_e32 v[36:37], v[4:5]
	v_mov_b64_e32 v[44:45], v[8:9]
	v_mov_b64_e32 v[64:65], v[24:25]
	v_mov_b64_e32 v[54:55], v[30:31]
	v_mov_b64_e32 v[58:59], v[26:27]
	v_mov_b64_e32 v[50:51], v[18:19]
	v_mov_b64_e32 v[38:39], v[10:11]
	v_mov_b64_e32 v[46:47], v[14:15]
	v_mov_b64_e32 v[34:35], v[2:3]
	v_mov_b64_e32 v[42:43], v[6:7]
	v_mov_b64_e32 v[62:63], v[22:23]
	v_mov_b64_e32 v[30:31], v[94:95]
	v_mov_b64_e32 v[26:27], v[90:91]
	v_mov_b64_e32 v[18:19], v[86:87]
	v_mov_b64_e32 v[10:11], v[82:83]
	v_mov_b64_e32 v[14:15], v[74:75]
	v_mov_b64_e32 v[2:3], v[66:67]
	v_mov_b64_e32 v[6:7], v[70:71]
	v_mov_b64_e32 v[22:23], v[78:79]
	s_cmpk_lt_i32 s7, 0x800
	v_mov_b64_e32 v[32:33], v[96:97]
	v_mov_b64_e32 v[28:29], v[92:93]
	v_mov_b64_e32 v[20:21], v[88:89]
	v_mov_b64_e32 v[12:13], v[84:85]
	v_mov_b64_e32 v[16:17], v[76:77]
	v_mov_b64_e32 v[4:5], v[68:69]
	v_mov_b64_e32 v[8:9], v[72:73]
	v_mov_b64_e32 v[24:25], v[80:81]
	s_mov_b32 s3, s7
	s_cbranch_scc0 .LBB0_78
.LBB0_76:
	s_add_i32 s7, s6, s3
	s_cmpk_gt_i32 s7, 0x7ff
	s_cbranch_scc1 .LBB0_75
	s_ashr_i32 s8, s7, 31
	s_lshr_b32 s8, s8, 26
	s_add_i32 s9, s7, s8
	s_ashr_i32 s8, s9, 6
	s_and_b32 s9, s9, 0xffc0
	s_sub_i32 s7, s7, s9
	s_bfe_i32 s9, s7, 0x80000
	s_bfe_u32 s9, s9, 0x2000d
	s_add_i32 s9, s7, s9
	s_bfe_i32 s10, s9, 0x80000
	s_and_b32 s9, s9, 0xfc
	s_sub_i32 s7, s7, s9
	s_ashr_i32 s9, s8, 31
	s_lshl_b64 s[8:9], s[8:9], 22
	s_sext_i32_i16 s10, s10
	s_sext_i32_i8 s7, s7
	s_add_u32 s8, s72, s8
	v_lshl_or_b32 v66, s7, 8, v99
	s_addc_u32 s9, s73, s9
	s_lshl_b32 s7, s10, 4
	s_andn2_b32 s7, s7, 63
	v_or_b32_e32 v68, s7, v110
	v_ashrrev_i32_e32 v69, 31, v68
	v_lshlrev_b64 v[68:69], 12, v[68:69]
	v_lshl_add_u64 v[68:69], s[8:9], 0, v[68:69]
	v_ashrrev_i32_e32 v67, 31, v66
	v_lshl_add_u64 v[90:91], v[66:67], 2, v[68:69]
	v_add_co_u32_e32 v66, vcc, s0, v90
	s_nop 1
	v_addc_co_u32_e32 v67, vcc, 0, v91, vcc
	v_add_co_u32_e32 v74, vcc, s1, v90
	global_load_dwordx4 v[70:73], v[66:67], off offset:-4096 nt
	s_nop 0
	global_load_dwordx4 v[66:69], v[66:67], off nt
	v_addc_co_u32_e32 v75, vcc, 0, v91, vcc
	v_add_co_u32_e32 v82, vcc, 0x4000, v90
	global_load_dwordx4 v[78:81], v[90:91], off nt
	s_nop 0
	global_load_dwordx4 v[74:77], v[74:75], off nt
	v_addc_co_u32_e32 v83, vcc, 0, v91, vcc
	v_add_co_u32_e32 v86, vcc, 0x5000, v90
	s_nop 1
	v_addc_co_u32_e32 v87, vcc, 0, v91, vcc
	v_add_co_u32_e32 v92, vcc, 0x6000, v90
	global_load_dwordx4 v[82:85], v[82:83], off nt
	s_nop 0
	global_load_dwordx4 v[86:89], v[86:87], off nt
	v_addc_co_u32_e32 v93, vcc, 0, v91, vcc
	v_add_co_u32_e32 v94, vcc, 0x7000, v90
	s_nop 1
	v_addc_co_u32_e32 v95, vcc, 0, v91, vcc
	global_load_dwordx4 v[90:93], v[92:93], off nt
	s_nop 0
	global_load_dwordx4 v[94:97], v[94:95], off nt
	s_branch .LBB0_75

; #define SEAM(k) do { if (IN(k) && IN((k) + 1)) xcd_barrier(bar); \
;         if (PROBE_MASK) { const unsigned long long t_ = __builtin_amdgcn_s_memrealtime(); if ((PROBE_MASK >> (k)) & 1u) pr_acc += t_ - pr_t0; pr_t0 = t_; } } while (0)
; __device__ __forceinline__ void convert_deferred(const Ptrs& P, unsigned char* lds, int quota) {
;     const int tid = threadIdx.x, wid = tid >> 6, lane = tid & 63;
;     float* tile = (float*)lds;
;     volatile __attribute__((address_space(3))) int* slot = (volatile __attribute__((address_space(3))) int*)((__attribute__((address_space(3))) unsigned char*)lds + 131072 + 320 + 11000);
;     unsigned* q = (unsigned*)(P.ws + WS_CTL) + CW_DEFQ;
;     for (int n = 0; n < quota; ++n) {
;         __syncthreads();
;         if (tid == 0) *slot = (int)atomicAdd(q, 1u);
;         __syncthreads();
;         const int t = *slot;
;         if (t >= DEF_GU + DEF_DN) break;
;         const bool gu = t < DEF_GU;
;         const float* src = gu ? P.in[34] : P.in[36]; bf16* dst = (bf16*)(P.ws + (gu ? WS_WGU : WS_WDN));
;         const int N = gu ? 2048 : 1024, ntn = N / 256, it = gu ? 2 * NE * 16 * 8 - DEF_GU + t : 2 * NE * 16 * 4 - DEF_DN + (t - DEF_GU);
; __global__ void __launch_bounds__(NT, 2) mega(Args args) {
;     ...
;         if (IDLE_LAST(68 * 7)) convert_deferred(P, lds, 4); } SEAM(2);
.LBB0_779:
	s_abs_i32 s3, s62
	v_cvt_f32_u32_e32 v2, s3
	s_sub_i32 s4, 0, s3
	s_mov_b32 s5, 0
	v_rcp_iflag_f32_e32 v2, v2
	s_nop 0
	v_mul_f32_e32 v2, 0x4f7ffffe, v2
	v_cvt_u32_f32_e32 v2, v2
	s_nop 0
	v_readfirstlane_b32 s6, v2
	s_mul_i32 s4, s4, s6
	s_mul_hi_u32 s4, s6, s4
	s_add_i32 s6, s6, s4
	s_mul_hi_u32 s4, s6, 0x1dc
	s_mul_i32 s4, s4, s3
	s_sub_i32 s4, 0x1dc, s4
	s_sub_i32 s6, s4, s3
	s_cmp_ge_u32 s4, s3
	s_cselect_b32 s4, s6, s4
	s_sub_i32 s6, s4, s3
	s_cmp_ge_u32 s4, s3
	s_cselect_b32 s3, s6, s4
	s_cmp_eq_u32 s3, 0
	s_cselect_b64 s[6:7], -1, 0
	s_cmp_lt_i32 s2, s3
	s_cselect_b64 s[8:9], -1, 0
	s_or_b64 s[6:7], s[6:7], s[8:9]
	s_and_b64 vcc, exec, s[6:7]
	s_cbranch_vccnz .LBB0_789
	v_and_b32_e32 v2, 0x7c, v155
	v_lshlrev_b32_e32 v3, 5, v0
	s_movk_i32 s3, 0x400
	v_lshrrev_b32_e32 v4, 6, v0
	v_and_or_b32 v12, v3, s3, v2
	v_bfe_u32 v2, v0, 3, 3
	v_lshl_or_b32 v5, v4, 5, v2
	v_lshlrev_b32_e32 v2, 3, v0
	v_lshl_add_u32 v11, v182, 4, 0
	v_and_b32_e32 v2, 56, v2
	v_mul_u32_u24_e32 v16, 0x2020, v4
	v_mov_b32_e32 v3, 0
	v_lshl_add_u32 v27, v5, 2, 0
	v_mul_u32_u24_e32 v28, 0x404, v2
	v_lshlrev_b32_e32 v10, 6, v5
	s_add_i32 s12, 0, 0x22c38
	v_add_u32_e32 v16, v11, v16
	v_and_b32_e32 v13, 0xfc, v155
	v_and_b32_e32 v14, 56, v154
	s_mov_b32 s3, 6
	v_or_b32_e32 v4, 0x200, v10
	v_mov_b32_e32 v5, v3
	v_or_b32_e32 v6, 0x400, v10
	v_mov_b32_e32 v7, v3
	v_or_b32_e32 v8, 0x600, v10
	v_mov_b32_e32 v9, v3
	v_mov_b32_e32 v15, s12
	s_movk_i32 s13, 0x17ff
	s_movk_i32 s14, 0x800
	s_mov_b32 s15, 0x1104e000
	s_movk_i32 s16, -2048
	v_add_u32_e32 v17, 0x404, v16
	v_add_u32_e32 v18, 0x40c, v16
	v_add_u32_e32 v19, 0x808, v16
	v_add_u32_e32 v20, 0xc0c, v16
	v_add_u32_e32 v21, 0xc14, v16
	v_add_u32_e32 v22, 0x1414, v16
	v_add_u32_e32 v23, 0x141c, v16
	v_add_u32_e32 v24, 0x1818, v16
	v_add_u32_e32 v25, 0x1c1c, v16
	v_add_u32_e32 v26, 0x1c24, v16
	v_lshlrev_b32_e32 v2, 1, v2
	v_add_u32_e32 v27, v27, v28
	v_lshlrev_b32_e32 v10, 1, v10
	s_branch .LBB0_782

; __device__ __forceinline__ unsigned g8_cvt_pk(float lo, float hi) { unsigned r; asm volatile("v_cvt_pk_bf16_f32 %0, %1, %2" : "=v"(r) : "v"(lo), "v"(hi)); return r; }
; __device__ __forceinline__ void bt_load(const float* __restrict__ src, int N, int perm, int it, int ntn, f32x4 (&v)[8]) {
;     const int wid = threadIdx.x >> 6, lane = threadIdx.x & 63;
;     const int per = 16 * ntn, z = it / per, r = it % per, kt = r / ntn, nt = r % ntn;
;     const int np = nt * 256 + lane * 4;
;     const int sc = perm ? (nt * 128 + (lane & 31) * 4 + (lane >> 5) * 1024) : np;
;     const float* p = src + (size_t)z * 1024 * N + (size_t)(kt * 64 + wid * 8) * N + sc;
; #pragma unroll
;     for (int i = 0; i < 8; ++i) v[i] = __builtin_nontemporal_load((const f32x4*)(p + (size_t)i * N));
; }
; __device__ __forceinline__ void convert_deferred(const Ptrs& P, unsigned char* lds, int quota) {
;     ...
;         __syncthreads();
;         if (tid == 0) *slot = (int)atomicAdd(q, 1u);
;         __syncthreads();
;         const int t = *slot;
;         if (t >= DEF_GU + DEF_DN) break;
;         const bool gu = t < DEF_GU;
;         const float* src = gu ? P.in[34] : P.in[36]; bf16* dst = (bf16*)(P.ws + (gu ? WS_WGU : WS_WDN));
;         const int N = gu ? 2048 : 1024, ntn = N / 256, it = gu ? 2 * NE * 16 * 8 - DEF_GU + t : 2 * NE * 16 * 4 - DEF_DN + (t - DEF_GU);
;         f32x4 cur[8];
;         bt_load(src, N, gu ? 1 : 0, it, ntn, cur);
; #pragma unroll
;         for (int i = 0; i < 8; ++i) { float* tp = tile + (wid * 8 + i) * 257 + lane * 4; tp[0] = cur[i][0]; tp[1] = cur[i][1]; tp[2] = cur[i][2]; tp[3] = cur[i][3]; }
;         __syncthreads();
;         const int per = 16 * ntn, z = it / per, r = it % per, kt = r / ntn, nt = r % ntn;
;         bf16* d = dst + (size_t)z * N * 1024 + (((size_t)nt * 16 + kt) << 14);
;         const int kc = lane & 7;
; #pragma unroll
;         for (int pss = 0; pss < 4; ++pss) {
;             const int nn = wid * 32 + pss * 8 + (lane >> 3); float f[8];
; #pragma unroll
;             for (int j = 0; j < 8; ++j) f[j] = tile[(kc * 8 + j) * 257 + nn];
;             u32x4 w; w.x = g8_cvt_pk(f[0], f[1]); w.y = g8_cvt_pk(f[2], f[3]); w.z = g8_cvt_pk(f[4], f[5]); w.w = g8_cvt_pk(f[6], f[7]);
;             *(u32x4*)(d + nn * 64 + kc * 8) = w;
;         }
.LBB0_786:
	s_or_b64 exec, exec, s[6:7]
	s_waitcnt lgkmcnt(0)
	s_barrier
	ds_read_b32 v11, v15
	s_mov_b64 s[6:7], -1
	s_waitcnt lgkmcnt(0)
	v_cmp_lt_i32_e32 vcc, s13, v11
	v_readfirstlane_b32 s4, v11
	s_cbranch_vccnz .LBB0_781
	s_cmpk_gt_i32 s4, 0xfff
	s_cselect_b64 vcc, -1, 0
	s_and_b64 s[6:7], vcc, exec
	s_cselect_b32 s6, s15, 0x104e000
	s_cselect_b32 s11, 0x400, s14
	s_cselect_b32 s17, s73, s69
	s_cselect_b32 s20, s72, s68
	s_cselect_b32 s7, s16, 0x1000
	s_cselect_b32 s18, 20, 21
	s_cselect_b32 s21, 10, 11
	s_add_u32 s26, s78, s6
	s_addc_u32 s27, s79, 0
	s_lshr_b32 s8, s11, 4
	s_abs_i32 s6, s8
	v_cvt_f32_u32_e32 v11, s6
	s_sub_i32 s19, 0, s6
	s_add_i32 s7, s7, s4
	s_abs_i32 s9, s7
	v_rcp_iflag_f32_e32 v11, v11
	s_xor_b32 s4, s7, s8
	s_lshr_b32 s10, s11, 8
	s_ashr_i32 s4, s4, 31
	v_mul_f32_e32 v11, 0x4f7ffffe, v11
	v_cvt_u32_f32_e32 v11, v11
	s_nop 0
	v_readfirstlane_b32 s28, v11
	s_mul_i32 s19, s19, s28
	s_mul_hi_u32 s19, s28, s19
	s_add_i32 s28, s28, s19
	s_mul_hi_u32 s19, s9, s28
	s_mul_i32 s28, s19, s6
	s_sub_i32 s9, s9, s28
	s_add_i32 s28, s19, 1
	s_sub_i32 s29, s9, s6
	s_cmp_ge_u32 s9, s6
	s_cselect_b32 s19, s28, s19
	s_cselect_b32 s9, s29, s9
	s_add_i32 s28, s19, 1
	s_cmp_ge_u32 s9, s6
	s_cselect_b32 s6, s28, s19
	s_xor_b32 s6, s6, s4
	s_sub_i32 s6, s6, s4
	s_sext_i32_i8 s4, s10
	v_cvt_f32_i32_e32 v11, s4
	s_mul_i32 s8, s6, s8
	s_sub_i32 s7, s7, s8
	v_cvt_f32_i32_e32 v28, s7
	v_rcp_iflag_f32_e32 v29, v11
	s_xor_b32 s4, s7, s4
	s_ashr_i32 s4, s4, 30
	s_or_b32 s4, s4, 1
	v_mul_f32_e32 v29, v28, v29
	v_trunc_f32_e32 v29, v29
	v_fma_f32 v28, -v29, v11, v28
	v_cvt_i32_f32_e32 v29, v29
	v_cmp_ge_f32_e64 s[8:9], |v28|, |v11|
	s_and_b64 s[8:9], s[8:9], exec
	s_cselect_b32 s4, s4, 0
	v_readfirstlane_b32 s8, v29
	s_add_i32 s8, s8, s4
	s_mul_i32 s9, s8, s10
	s_sub_i32 s10, s7, s9
	s_sext_i32_i8 s7, s10
	v_lshl_add_u32 v11, s7, 7, v12
	v_lshl_or_b32 v28, s7, 8, v13
	s_ashr_i32 s7, s6, 31
	s_sext_i32_i8 s4, s8
	s_lshl_b64 s[18:19], s[6:7], s18
	v_lshl_or_b32 v30, s4, 6, v14
	s_lshl_b64 s[18:19], s[18:19], 2
	v_ashrrev_i32_e32 v31, 31, v30
	s_add_u32 s18, s20, s18
	v_cndmask_b32_e32 v28, v11, v28, vcc
	s_addc_u32 s19, s17, s19
	v_lshlrev_b64 v[30:31], s21, v[30:31]
	v_lshl_add_u64 v[30:31], v[30:31], 2, s[18:19]
	v_ashrrev_i32_e32 v29, 31, v28
	v_lshl_add_u64 v[52:53], v[28:29], 2, v[30:31]
	s_lshl_b64 s[18:19], 12, s21
	s_lshl_b32 s4, s11, 2
	v_lshl_add_u64 v[40:41], v[52:53], 0, s[18:19]
	s_lshl_b64 s[18:19], 24, s21
	v_lshl_add_u64 v[36:37], v[52:53], 0, s[4:5]
	v_lshl_add_u64 v[44:45], v[52:53], 0, s[18:19]
	s_lshl_b64 s[18:19], 28, s21
	v_lshl_add_u64 v[54:55], v[36:37], 0, s[4:5]
	v_lshl_add_u64 v[48:49], v[52:53], 0, s[18:19]
	s_lshl_b32 s4, s11, 3
	s_lshl_b64 s[18:19], 20, s21
	global_load_dwordx4 v[28:31], v[52:53], off nt
	global_load_dwordx4 v[32:35], v[36:37], off nt
	s_nop 0
	global_load_dwordx4 v[36:39], v[54:55], off nt
	s_nop 0
	global_load_dwordx4 v[40:43], v[40:41], off nt
	v_lshl_add_u64 v[54:55], v[54:55], 0, s[4:5]
	v_lshl_add_u64 v[56:57], v[52:53], 0, s[18:19]
	global_load_dwordx4 v[44:47], v[44:45], off nt
	s_nop 0
	global_load_dwordx4 v[48:51], v[48:49], off nt
	s_nop 0
	global_load_dwordx4 v[52:55], v[54:55], off nt
	s_nop 0
	global_load_dwordx4 v[56:59], v[56:57], off nt
	s_lshl_b64 s[6:7], s[6:7], s21
	s_lshl_b64 s[6:7], s[6:7], 11
	s_add_u32 s4, s26, s6
	s_addc_u32 s11, s27, s7
	s_bfe_i64 s[6:7], s[10:11], 0x80000
	s_bfe_i64 s[8:9], s[8:9], 0x80000
	s_lshl_b64 s[6:7], s[6:7], 19
	s_add_u32 s4, s4, s6
	s_addc_u32 s10, s11, s7
	s_lshl_b64 s[6:7], s[8:9], 15
	s_add_u32 s6, s4, s6
	s_addc_u32 s7, s10, s7
	v_mov_b32_e32 v11, v3
	s_add_i32 s3, s3, -1
	s_cmp_eq_u32 s3, 0
	s_waitcnt vmcnt(7)
	ds_write_b128 v16, v[28:31]
	s_waitcnt vmcnt(6)
	ds_write2_b32 v17, v32, v33 offset1:1
	ds_write2_b32 v18, v34, v35 offset1:1
	s_waitcnt vmcnt(3)
	ds_write2_b64 v24, v[44:45], v[46:47] offset1:1
	s_waitcnt vmcnt(2)
	ds_write2_b32 v25, v48, v49 offset1:1
	ds_write2_b32 v26, v50, v51 offset1:1
	ds_write2_b64 v19, v[36:37], v[38:39] offset1:1
	ds_write2_b32 v20, v40, v41 offset1:1
	ds_write2_b32 v21, v42, v43 offset1:1
	s_waitcnt vmcnt(1)
	ds_write_b128 v16, v[52:55] offset:4112
	s_waitcnt vmcnt(0)
	ds_write2_b32 v22, v56, v57 offset1:1
	ds_write2_b32 v23, v58, v59 offset1:1
	s_waitcnt lgkmcnt(0)
	s_barrier
	ds_read_b32 v28, v27 offset:1028
	ds_read_b32 v29, v27 offset:3084
	ds_read_b32 v30, v27 offset:5140
	ds_read_b32 v31, v27 offset:7196
	ds_read_b32 v32, v27 offset:6168
	ds_read_b32 v33, v27 offset:4112
	ds_read_b32 v34, v27 offset:2056
	ds_read_b32 v35, v27
	s_waitcnt lgkmcnt(0)
	v_cvt_pk_bf16_f32 v28, v35, v28
	v_cvt_pk_bf16_f32 v29, v34, v29
	v_cvt_pk_bf16_f32 v30, v33, v30
	v_cvt_pk_bf16_f32 v31, v32, v31
	ds_read_b32 v36, v27 offset:1060
	ds_read_b32 v37, v27 offset:3116
	ds_read_b32 v38, v27 offset:5172
	ds_read_b32 v39, v27 offset:7228
	ds_read_b32 v40, v27 offset:6200
	ds_read_b32 v41, v27 offset:4144
	ds_read_b32 v42, v27 offset:2088
	ds_read_b32 v43, v27 offset:32
	v_lshl_add_u64 v[32:33], s[6:7], 0, v[2:3]
	v_lshl_add_u64 v[34:35], v[32:33], 0, v[10:11]
	global_store_dwordx4 v[34:35], v[28:31], off
	v_lshl_add_u64 v[34:35], v[4:5], 1, v[32:33]
	s_cselect_b64 s[6:7], -1, 0
	s_waitcnt lgkmcnt(0)
	v_cvt_pk_bf16_f32 v28, v43, v36
	v_cvt_pk_bf16_f32 v29, v42, v37
	v_cvt_pk_bf16_f32 v30, v41, v38
	v_cvt_pk_bf16_f32 v31, v40, v39
	ds_read_b32 v11, v27 offset:1092
	ds_read_b32 v36, v27 offset:3148
	ds_read_b32 v37, v27 offset:6232
	ds_read_b32 v38, v27 offset:4176
	ds_read_b32 v39, v27 offset:2120
	ds_read_b32 v40, v27 offset:64
	ds_read_b32 v41, v27 offset:5204
	ds_read_b32 v42, v27 offset:7260
	global_store_dwordx4 v[34:35], v[28:31], off
	v_lshl_add_u64 v[34:35], v[6:7], 1, v[32:33]
	v_lshl_add_u64 v[32:33], v[8:9], 1, v[32:33]
	s_waitcnt lgkmcnt(2)
	v_cvt_pk_bf16_f32 v28, v40, v11
	v_cvt_pk_bf16_f32 v29, v39, v36
	s_waitcnt lgkmcnt(1)
	v_cvt_pk_bf16_f32 v30, v38, v41
	s_waitcnt lgkmcnt(0)
	v_cvt_pk_bf16_f32 v31, v37, v42
	ds_read_b32 v11, v27 offset:1124
	ds_read_b32 v36, v27 offset:3180
	ds_read_b32 v37, v27 offset:6264
	ds_read_b32 v38, v27 offset:4208
	ds_read_b32 v39, v27 offset:2152
	ds_read_b32 v40, v27 offset:96
	ds_read_b32 v41, v27 offset:5236
	ds_read_b32 v42, v27 offset:7292
	global_store_dwordx4 v[34:35], v[28:31], off
	s_waitcnt lgkmcnt(2)
	s_nop 0
	v_cvt_pk_bf16_f32 v28, v40, v11
	v_cvt_pk_bf16_f32 v29, v39, v36
	s_waitcnt lgkmcnt(1)
	v_cvt_pk_bf16_f32 v30, v38, v41
	s_waitcnt lgkmcnt(0)
	v_cvt_pk_bf16_f32 v31, v37, v42
	global_store_dwordx4 v[32:33], v[28:31], off
	s_branch .LBB0_781

; #define SEAM(k) do { if (IN(k) && IN((k) + 1)) xcd_barrier(bar); \
;         if (PROBE_MASK) { const unsigned long long t_ = __builtin_amdgcn_s_memrealtime(); if ((PROBE_MASK >> (k)) & 1u) pr_acc += t_ - pr_t0; pr_t0 = t_; } } while (0)
; __device__ __forceinline__ void convert_deferred(const Ptrs& P, unsigned char* lds, int quota) {
;     const int tid = threadIdx.x, wid = tid >> 6, lane = tid & 63;
;     float* tile = (float*)lds;
;     volatile __attribute__((address_space(3))) int* slot = (volatile __attribute__((address_space(3))) int*)((__attribute__((address_space(3))) unsigned char*)lds + 131072 + 320 + 11000);
;     unsigned* q = (unsigned*)(P.ws + WS_CTL) + CW_DEFQ;
;     for (int n = 0; n < quota; ++n) {
;         __syncthreads();
;         if (tid == 0) *slot = (int)atomicAdd(q, 1u);
;         __syncthreads();
;         const int t = *slot;
;         if (t >= DEF_GU + DEF_DN) break;
;         const bool gu = t < DEF_GU;
;         const float* src = gu ? P.in[34] : P.in[36]; bf16* dst = (bf16*)(P.ws + (gu ? WS_WGU : WS_WDN));
;         const int N = gu ? 2048 : 1024, ntn = N / 256, it = gu ? 2 * NE * 16 * 8 - DEF_GU + t : 2 * NE * 16 * 4 - DEF_DN + (t - DEF_GU);
; __global__ void __launch_bounds__(NT, 2) mega(Args args) {
;     ...
;         if (IDLE_LAST(68 * 4)) convert_deferred(P, lds, 4); } SEAM(6);
.LBB0_1286:
	s_abs_i32 s3, s62
	v_cvt_f32_u32_e32 v2, s3
	s_sub_i32 s4, 0, s3
	s_mov_b32 s5, 0
	v_rcp_iflag_f32_e32 v2, v2
	s_nop 0
	v_mul_f32_e32 v2, 0x4f7ffffe, v2
	v_cvt_u32_f32_e32 v2, v2
	s_nop 0
	v_readfirstlane_b32 s6, v2
	s_mul_i32 s4, s4, s6
	s_mul_hi_u32 s4, s6, s4
	s_add_i32 s6, s6, s4
	s_mul_hi_u32 s4, s6, 0x110
	s_mul_i32 s4, s4, s3
	s_sub_i32 s4, 0x110, s4
	s_sub_i32 s6, s4, s3
	s_cmp_ge_u32 s4, s3
	s_cselect_b32 s4, s6, s4
	s_sub_i32 s6, s4, s3
	s_cmp_ge_u32 s4, s3
	s_cselect_b32 s3, s6, s4
	s_cmp_eq_u32 s3, 0
	s_cselect_b64 s[6:7], -1, 0
	s_cmp_lt_i32 s2, s3
	s_cselect_b64 s[8:9], -1, 0
	s_or_b64 s[6:7], s[6:7], s[8:9]
	s_and_b64 vcc, exec, s[6:7]
	s_cbranch_vccnz .LBB0_1296
	v_and_b32_e32 v2, 0x7c, v188
	v_lshlrev_b32_e32 v3, 5, v0
	s_movk_i32 s3, 0x400
	v_and_or_b32 v12, v3, s3, v2
	v_bfe_u32 v2, v0, 3, 3
	v_lshl_or_b32 v4, v1, 5, v2
	v_lshlrev_b32_e32 v2, 3, v0
	v_lshl_add_u32 v11, v182, 4, 0
	v_and_b32_e32 v2, 56, v2
	v_mul_u32_u24_e32 v16, 0x2020, v1
	v_mov_b32_e32 v3, 0
	v_lshl_add_u32 v27, v4, 2, 0
	v_mul_u32_u24_e32 v28, 0x404, v2
	v_lshlrev_b32_e32 v10, 6, v4
	s_add_i32 s12, 0, 0x22c38
	v_add_u32_e32 v16, v11, v16
	v_and_b32_e32 v13, 0xfc, v188
	v_and_b32_e32 v14, 56, v185
	s_mov_b32 s3, 10
	v_or_b32_e32 v4, 0x200, v10
	v_mov_b32_e32 v5, v3
	v_or_b32_e32 v6, 0x400, v10
	v_mov_b32_e32 v7, v3
	v_or_b32_e32 v8, 0x600, v10
	v_mov_b32_e32 v9, v3
	v_mov_b32_e32 v15, s12
	s_movk_i32 s13, 0x17ff
	s_movk_i32 s14, 0x800
	s_mov_b32 s15, 0x1104e000
	s_movk_i32 s16, -2048
	v_add_u32_e32 v17, 0x404, v16
	v_add_u32_e32 v18, 0x40c, v16
	v_add_u32_e32 v19, 0x808, v16
	v_add_u32_e32 v20, 0xc0c, v16
	v_add_u32_e32 v21, 0xc14, v16
	v_add_u32_e32 v22, 0x1414, v16
	v_add_u32_e32 v23, 0x141c, v16
	v_add_u32_e32 v24, 0x1818, v16
	v_add_u32_e32 v25, 0x1c1c, v16
	v_add_u32_e32 v26, 0x1c24, v16
	v_lshlrev_b32_e32 v2, 1, v2
	v_add_u32_e32 v27, v27, v28
	v_lshlrev_b32_e32 v10, 1, v10
	s_branch .LBB0_1289

; __device__ __forceinline__ unsigned g8_cvt_pk(float lo, float hi) { unsigned r; asm volatile("v_cvt_pk_bf16_f32 %0, %1, %2" : "=v"(r) : "v"(lo), "v"(hi)); return r; }
; __device__ __forceinline__ void bt_load(const float* __restrict__ src, int N, int perm, int it, int ntn, f32x4 (&v)[8]) {
;     const int wid = threadIdx.x >> 6, lane = threadIdx.x & 63;
;     const int per = 16 * ntn, z = it / per, r = it % per, kt = r / ntn, nt = r % ntn;
;     const int np = nt * 256 + lane * 4;
;     const int sc = perm ? (nt * 128 + (lane & 31) * 4 + (lane >> 5) * 1024) : np;
;     const float* p = src + (size_t)z * 1024 * N + (size_t)(kt * 64 + wid * 8) * N + sc;
; #pragma unroll
;     for (int i = 0; i < 8; ++i) v[i] = __builtin_nontemporal_load((const f32x4*)(p + (size_t)i * N));
; }
; __device__ __forceinline__ void convert_deferred(const Ptrs& P, unsigned char* lds, int quota) {
;     ...
;         __syncthreads();
;         if (tid == 0) *slot = (int)atomicAdd(q, 1u);
;         __syncthreads();
;         const int t = *slot;
;         if (t >= DEF_GU + DEF_DN) break;
;         const bool gu = t < DEF_GU;
;         const float* src = gu ? P.in[34] : P.in[36]; bf16* dst = (bf16*)(P.ws + (gu ? WS_WGU : WS_WDN));
;         const int N = gu ? 2048 : 1024, ntn = N / 256, it = gu ? 2 * NE * 16 * 8 - DEF_GU + t : 2 * NE * 16 * 4 - DEF_DN + (t - DEF_GU);
;         f32x4 cur[8];
;         bt_load(src, N, gu ? 1 : 0, it, ntn, cur);
; #pragma unroll
;         for (int i = 0; i < 8; ++i) { float* tp = tile + (wid * 8 + i) * 257 + lane * 4; tp[0] = cur[i][0]; tp[1] = cur[i][1]; tp[2] = cur[i][2]; tp[3] = cur[i][3]; }
;         __syncthreads();
;         const int per = 16 * ntn, z = it / per, r = it % per, kt = r / ntn, nt = r % ntn;
;         bf16* d = dst + (size_t)z * N * 1024 + (((size_t)nt * 16 + kt) << 14);
;         const int kc = lane & 7;
; #pragma unroll
;         for (int pss = 0; pss < 4; ++pss) {
;             const int nn = wid * 32 + pss * 8 + (lane >> 3); float f[8];
; #pragma unroll
;             for (int j = 0; j < 8; ++j) f[j] = tile[(kc * 8 + j) * 257 + nn];
;             u32x4 w; w.x = g8_cvt_pk(f[0], f[1]); w.y = g8_cvt_pk(f[2], f[3]); w.z = g8_cvt_pk(f[4], f[5]); w.w = g8_cvt_pk(f[6], f[7]);
;             *(u32x4*)(d + nn * 64 + kc * 8) = w;
;         }
.LBB0_1293:
	s_or_b64 exec, exec, s[6:7]
	s_waitcnt lgkmcnt(0)
	s_barrier
	ds_read_b32 v11, v15
	s_mov_b64 s[6:7], -1
	s_waitcnt lgkmcnt(0)
	v_cmp_lt_i32_e32 vcc, s13, v11
	v_readfirstlane_b32 s4, v11
	s_cbranch_vccnz .LBB0_1288
	s_cmpk_gt_i32 s4, 0xfff
	s_cselect_b64 vcc, -1, 0
	s_and_b64 s[6:7], vcc, exec
	s_cselect_b32 s6, s15, 0x104e000
	s_cselect_b32 s11, 0x400, s14
	s_cselect_b32 s17, s73, s69
	s_cselect_b32 s20, s72, s68
	s_cselect_b32 s7, s16, 0x1000
	s_cselect_b32 s18, 20, 21
	s_cselect_b32 s21, 10, 11
	s_add_u32 s22, s78, s6
	s_addc_u32 s23, s79, 0
	s_lshr_b32 s8, s11, 4
	s_abs_i32 s6, s8
	v_cvt_f32_u32_e32 v11, s6
	s_sub_i32 s19, 0, s6
	s_add_i32 s7, s7, s4
	s_abs_i32 s9, s7
	v_rcp_iflag_f32_e32 v11, v11
	s_xor_b32 s4, s7, s8
	s_lshr_b32 s10, s11, 8
	s_ashr_i32 s4, s4, 31
	v_mul_f32_e32 v11, 0x4f7ffffe, v11
	v_cvt_u32_f32_e32 v11, v11
	s_nop 0
	v_readfirstlane_b32 s24, v11
	s_mul_i32 s19, s19, s24
	s_mul_hi_u32 s19, s24, s19
	s_add_i32 s24, s24, s19
	s_mul_hi_u32 s19, s9, s24
	s_mul_i32 s24, s19, s6
	s_sub_i32 s9, s9, s24
	s_add_i32 s24, s19, 1
	s_sub_i32 s25, s9, s6
	s_cmp_ge_u32 s9, s6
	s_cselect_b32 s19, s24, s19
	s_cselect_b32 s9, s25, s9
	s_add_i32 s24, s19, 1
	s_cmp_ge_u32 s9, s6
	s_cselect_b32 s6, s24, s19
	s_xor_b32 s6, s6, s4
	s_sub_i32 s6, s6, s4
	s_sext_i32_i8 s4, s10
	v_cvt_f32_i32_e32 v11, s4
	s_mul_i32 s8, s6, s8
	s_sub_i32 s7, s7, s8
	v_cvt_f32_i32_e32 v28, s7
	v_rcp_iflag_f32_e32 v29, v11
	s_xor_b32 s4, s7, s4
	s_ashr_i32 s4, s4, 30
	s_or_b32 s4, s4, 1
	v_mul_f32_e32 v29, v28, v29
	v_trunc_f32_e32 v29, v29
	v_fma_f32 v28, -v29, v11, v28
	v_cvt_i32_f32_e32 v29, v29
	v_cmp_ge_f32_e64 s[8:9], |v28|, |v11|
	s_and_b64 s[8:9], s[8:9], exec
	s_cselect_b32 s4, s4, 0
	v_readfirstlane_b32 s8, v29
	s_add_i32 s8, s8, s4
	s_mul_i32 s9, s8, s10
	s_sub_i32 s10, s7, s9
	s_sext_i32_i8 s7, s10
	v_lshl_add_u32 v11, s7, 7, v12
	v_lshl_or_b32 v28, s7, 8, v13
	s_ashr_i32 s7, s6, 31
	s_sext_i32_i8 s4, s8
	s_lshl_b64 s[18:19], s[6:7], s18
	v_lshl_or_b32 v30, s4, 6, v14
	s_lshl_b64 s[18:19], s[18:19], 2
	v_ashrrev_i32_e32 v31, 31, v30
	s_add_u32 s18, s20, s18
	v_cndmask_b32_e32 v28, v11, v28, vcc
	s_addc_u32 s19, s17, s19
	v_lshlrev_b64 v[30:31], s21, v[30:31]
	v_lshl_add_u64 v[30:31], v[30:31], 2, s[18:19]
	v_ashrrev_i32_e32 v29, 31, v28
	v_lshl_add_u64 v[52:53], v[28:29], 2, v[30:31]
	s_lshl_b64 s[18:19], 12, s21
	s_lshl_b32 s4, s11, 2
	v_lshl_add_u64 v[40:41], v[52:53], 0, s[18:19]
	s_lshl_b64 s[18:19], 24, s21
	v_lshl_add_u64 v[36:37], v[52:53], 0, s[4:5]
	v_lshl_add_u64 v[44:45], v[52:53], 0, s[18:19]
	s_lshl_b64 s[18:19], 28, s21
	v_lshl_add_u64 v[54:55], v[36:37], 0, s[4:5]
	v_lshl_add_u64 v[48:49], v[52:53], 0, s[18:19]
	s_lshl_b32 s4, s11, 3
	s_lshl_b64 s[18:19], 20, s21
	global_load_dwordx4 v[28:31], v[52:53], off nt
	global_load_dwordx4 v[32:35], v[36:37], off nt
	s_nop 0
	global_load_dwordx4 v[36:39], v[54:55], off nt
	s_nop 0
	global_load_dwordx4 v[40:43], v[40:41], off nt
	v_lshl_add_u64 v[54:55], v[54:55], 0, s[4:5]
	v_lshl_add_u64 v[56:57], v[52:53], 0, s[18:19]
	global_load_dwordx4 v[44:47], v[44:45], off nt
	s_nop 0
	global_load_dwordx4 v[48:51], v[48:49], off nt
	s_nop 0
	global_load_dwordx4 v[52:55], v[54:55], off nt
	s_nop 0
	global_load_dwordx4 v[56:59], v[56:57], off nt
	s_lshl_b64 s[6:7], s[6:7], s21
	s_lshl_b64 s[6:7], s[6:7], 11
	s_add_u32 s4, s22, s6
	s_addc_u32 s11, s23, s7
	s_bfe_i64 s[6:7], s[10:11], 0x80000
	s_bfe_i64 s[8:9], s[8:9], 0x80000
	s_lshl_b64 s[6:7], s[6:7], 19
	s_add_u32 s4, s4, s6
	s_addc_u32 s10, s11, s7
	s_lshl_b64 s[6:7], s[8:9], 15
	s_add_u32 s6, s4, s6
	s_addc_u32 s7, s10, s7
	v_mov_b32_e32 v11, v3
	s_add_i32 s3, s3, -1
	s_cmp_eq_u32 s3, 0
	s_waitcnt vmcnt(7)
	ds_write_b128 v16, v[28:31]
	s_waitcnt vmcnt(6)
	ds_write2_b32 v17, v32, v33 offset1:1
	ds_write2_b32 v18, v34, v35 offset1:1
	s_waitcnt vmcnt(3)
	ds_write2_b64 v24, v[44:45], v[46:47] offset1:1
	s_waitcnt vmcnt(2)
	ds_write2_b32 v25, v48, v49 offset1:1
	ds_write2_b32 v26, v50, v51 offset1:1
	ds_write2_b64 v19, v[36:37], v[38:39] offset1:1
	ds_write2_b32 v20, v40, v41 offset1:1
	ds_write2_b32 v21, v42, v43 offset1:1
	s_waitcnt vmcnt(1)
	ds_write_b128 v16, v[52:55] offset:4112
	s_waitcnt vmcnt(0)
	ds_write2_b32 v22, v56, v57 offset1:1
	ds_write2_b32 v23, v58, v59 offset1:1
	s_waitcnt lgkmcnt(0)
	s_barrier
	ds_read_b32 v28, v27 offset:1028
	ds_read_b32 v29, v27 offset:3084
	ds_read_b32 v30, v27 offset:5140
	ds_read_b32 v31, v27 offset:7196
	ds_read_b32 v32, v27 offset:6168
	ds_read_b32 v33, v27 offset:4112
	ds_read_b32 v34, v27 offset:2056
	ds_read_b32 v35, v27
	s_waitcnt lgkmcnt(0)
	v_cvt_pk_bf16_f32 v28, v35, v28
	v_cvt_pk_bf16_f32 v29, v34, v29
	v_cvt_pk_bf16_f32 v30, v33, v30
	v_cvt_pk_bf16_f32 v31, v32, v31
	ds_read_b32 v36, v27 offset:1060
	ds_read_b32 v37, v27 offset:3116
	ds_read_b32 v38, v27 offset:5172
	ds_read_b32 v39, v27 offset:7228
	ds_read_b32 v40, v27 offset:6200
	ds_read_b32 v41, v27 offset:4144
	ds_read_b32 v42, v27 offset:2088
	ds_read_b32 v43, v27 offset:32
	v_lshl_add_u64 v[32:33], s[6:7], 0, v[2:3]
	v_lshl_add_u64 v[34:35], v[32:33], 0, v[10:11]
	global_store_dwordx4 v[34:35], v[28:31], off
	v_lshl_add_u64 v[34:35], v[4:5], 1, v[32:33]
	s_cselect_b64 s[6:7], -1, 0
	s_waitcnt lgkmcnt(0)
	v_cvt_pk_bf16_f32 v28, v43, v36
	v_cvt_pk_bf16_f32 v29, v42, v37
	v_cvt_pk_bf16_f32 v30, v41, v38
	v_cvt_pk_bf16_f32 v31, v40, v39
	ds_read_b32 v11, v27 offset:1092
	ds_read_b32 v36, v27 offset:3148
	ds_read_b32 v37, v27 offset:6232
	ds_read_b32 v38, v27 offset:4176
	ds_read_b32 v39, v27 offset:2120
	ds_read_b32 v40, v27 offset:64
	ds_read_b32 v41, v27 offset:5204
	ds_read_b32 v42, v27 offset:7260
	global_store_dwordx4 v[34:35], v[28:31], off
	v_lshl_add_u64 v[34:35], v[6:7], 1, v[32:33]
	v_lshl_add_u64 v[32:33], v[8:9], 1, v[32:33]
	s_waitcnt lgkmcnt(2)
	v_cvt_pk_bf16_f32 v28, v40, v11
	v_cvt_pk_bf16_f32 v29, v39, v36
	s_waitcnt lgkmcnt(1)
	v_cvt_pk_bf16_f32 v30, v38, v41
	s_waitcnt lgkmcnt(0)
	v_cvt_pk_bf16_f32 v31, v37, v42
	ds_read_b32 v11, v27 offset:1124
	ds_read_b32 v36, v27 offset:3180
	ds_read_b32 v37, v27 offset:6264
	ds_read_b32 v38, v27 offset:4208
	ds_read_b32 v39, v27 offset:2152
	ds_read_b32 v40, v27 offset:96
	ds_read_b32 v41, v27 offset:5236
	ds_read_b32 v42, v27 offset:7292
	global_store_dwordx4 v[34:35], v[28:31], off
	s_waitcnt lgkmcnt(2)
	s_nop 0
	v_cvt_pk_bf16_f32 v28, v40, v11
	v_cvt_pk_bf16_f32 v29, v39, v36
	s_waitcnt lgkmcnt(1)
	v_cvt_pk_bf16_f32 v30, v38, v41
	s_waitcnt lgkmcnt(0)
	v_cvt_pk_bf16_f32 v31, v37, v42
	global_store_dwordx4 v[32:33], v[28:31], off
	s_branch .LBB0_1288

; #define LAS __attribute__((address_space(3)))
; #define SEAM(k) do { if (IN(k) && IN((k) + 1)) xcd_barrier(bar); \
;         if (PROBE_MASK) { const unsigned long long t_ = __builtin_amdgcn_s_memrealtime(); if ((PROBE_MASK >> (k)) & 1u) pr_acc += t_ - pr_t0; pr_t0 = t_; } } while (0)
; __device__ __forceinline__ void convert_deferred(const Ptrs& P, unsigned char* lds, int quota) {
;     const int tid = threadIdx.x, wid = tid >> 6, lane = tid & 63;
;     float* tile = (float*)lds;
;     volatile __attribute__((address_space(3))) int* slot = (volatile __attribute__((address_space(3))) int*)((__attribute__((address_space(3))) unsigned char*)lds + 131072 + 320 + 11000);
;     unsigned* q = (unsigned*)(P.ws + WS_CTL) + CW_DEFQ;
;     for (int n = 0; n < quota; ++n) {
;         __syncthreads();
;         if (tid == 0) *slot = (int)atomicAdd(q, 1u);
;         __syncthreads();
;         const int t = *slot;
;         if (t >= DEF_GU + DEF_DN) break;
;         const bool gu = t < DEF_GU;
;         const float* src = gu ? P.in[34] : P.in[36]; bf16* dst = (bf16*)(P.ws + (gu ? WS_WGU : WS_WDN));
;         const int N = gu ? 2048 : 1024, ntn = N / 256, it = gu ? 2 * NE * 16 * 8 - DEF_GU + t : 2 * NE * 16 * 4 - DEF_DN + (t - DEF_GU);
; __global__ void __launch_bounds__(NT, 2) mega(Args args) {
;     ...
;         { const int rem_ = ((LAS int*)(LDSP + MISC_OFF + 256))[96] % G; if (rem_ != 0 && vcu >= rem_) convert_deferred(P, lds, 5); } } SEAM(9);
.LBB0_1609:
	s_abs_i32 s0, s62
	v_cvt_f32_u32_e32 v2, s0
	s_sub_i32 s5, 0, s0
	s_abs_i32 s4, s9
	s_ashr_i32 s3, s9, 31
	v_rcp_iflag_f32_e32 v2, v2
	s_mov_b32 s1, 0
	v_mul_f32_e32 v2, 0x4f7ffffe, v2
	v_cvt_u32_f32_e32 v2, v2
	s_nop 0
	v_readfirstlane_b32 s6, v2
	s_mul_i32 s5, s5, s6
	s_mul_hi_u32 s5, s6, s5
	s_add_i32 s6, s6, s5
	s_mul_hi_u32 s5, s4, s6
	s_mul_i32 s5, s5, s0
	s_sub_i32 s4, s4, s5
	s_sub_i32 s5, s4, s0
	s_cmp_ge_u32 s4, s0
	s_cselect_b32 s4, s5, s4
	s_sub_i32 s5, s4, s0
	s_cmp_ge_u32 s4, s0
	s_cselect_b32 s0, s5, s4
	s_xor_b32 s0, s0, s3
	s_sub_i32 s0, s0, s3
	s_cmp_eq_u32 s0, 0
	v_readlane_b32 s3, v254, 2
	s_cselect_b64 s[4:5], -1, 0
	s_cmp_lt_i32 s3, s0
	s_cselect_b64 s[6:7], -1, 0
	s_or_b64 s[4:5], s[4:5], s[6:7]
	s_and_b64 vcc, exec, s[4:5]
	s_cbranch_vccnz .LBB0_1619
	v_and_b32_e32 v2, 0x7c, v175
	v_lshlrev_b32_e32 v3, 5, v0
	s_movk_i32 s0, 0x400
	v_and_or_b32 v12, v3, s0, v2
	v_bfe_u32 v2, v0, 3, 3
	v_lshl_or_b32 v4, v1, 5, v2
	v_lshlrev_b32_e32 v2, 3, v0
	v_lshl_add_u32 v11, v182, 4, 0
	v_and_b32_e32 v2, 56, v2
	v_mul_u32_u24_e32 v16, 0x2020, v1
	v_mov_b32_e32 v3, 0
	v_lshl_add_u32 v27, v4, 2, 0
	v_mul_u32_u24_e32 v28, 0x404, v2
	v_lshlrev_b32_e32 v10, 6, v4
	s_add_i32 s10, 0, 0x22c38
	v_add_u32_e32 v16, v11, v16
	s_mov_b32 s3, 9
	v_and_b32_e32 v13, 0xfc, v175
	v_and_b32_e32 v14, 56, v173
	v_or_b32_e32 v4, 0x200, v10
	v_mov_b32_e32 v5, v3
	v_or_b32_e32 v6, 0x400, v10
	v_mov_b32_e32 v7, v3
	v_or_b32_e32 v8, 0x600, v10
	v_mov_b32_e32 v9, v3
	v_mov_b32_e32 v15, s10
	s_movk_i32 s11, 0x17ff
	s_movk_i32 s12, 0x800
	s_mov_b32 s13, 0x1104e000
	s_movk_i32 s14, -2048
	v_add_u32_e32 v17, 0x404, v16
	v_add_u32_e32 v18, 0x40c, v16
	v_add_u32_e32 v19, 0x808, v16
	v_add_u32_e32 v20, 0xc0c, v16
	v_add_u32_e32 v21, 0xc14, v16
	v_add_u32_e32 v22, 0x1414, v16
	v_add_u32_e32 v23, 0x141c, v16
	v_add_u32_e32 v24, 0x1818, v16
	v_add_u32_e32 v25, 0x1c1c, v16
	v_add_u32_e32 v26, 0x1c24, v16
	v_lshlrev_b32_e32 v2, 1, v2
	v_add_u32_e32 v27, v27, v28
	v_lshlrev_b32_e32 v10, 1, v10
	s_branch .LBB0_1612

; __device__ __forceinline__ unsigned g8_cvt_pk(float lo, float hi) { unsigned r; asm volatile("v_cvt_pk_bf16_f32 %0, %1, %2" : "=v"(r) : "v"(lo), "v"(hi)); return r; }
; __device__ __forceinline__ void bt_load(const float* __restrict__ src, int N, int perm, int it, int ntn, f32x4 (&v)[8]) {
;     const int wid = threadIdx.x >> 6, lane = threadIdx.x & 63;
;     const int per = 16 * ntn, z = it / per, r = it % per, kt = r / ntn, nt = r % ntn;
;     const int np = nt * 256 + lane * 4;
;     const int sc = perm ? (nt * 128 + (lane & 31) * 4 + (lane >> 5) * 1024) : np;
;     const float* p = src + (size_t)z * 1024 * N + (size_t)(kt * 64 + wid * 8) * N + sc;
; #pragma unroll
;     for (int i = 0; i < 8; ++i) v[i] = __builtin_nontemporal_load((const f32x4*)(p + (size_t)i * N));
; }
; __device__ __forceinline__ void convert_deferred(const Ptrs& P, unsigned char* lds, int quota) {
;     ...
;         __syncthreads();
;         if (tid == 0) *slot = (int)atomicAdd(q, 1u);
;         __syncthreads();
;         const int t = *slot;
;         if (t >= DEF_GU + DEF_DN) break;
;         const bool gu = t < DEF_GU;
;         const float* src = gu ? P.in[34] : P.in[36]; bf16* dst = (bf16*)(P.ws + (gu ? WS_WGU : WS_WDN));
;         const int N = gu ? 2048 : 1024, ntn = N / 256, it = gu ? 2 * NE * 16 * 8 - DEF_GU + t : 2 * NE * 16 * 4 - DEF_DN + (t - DEF_GU);
;         f32x4 cur[8];
;         bt_load(src, N, gu ? 1 : 0, it, ntn, cur);
; #pragma unroll
;         for (int i = 0; i < 8; ++i) { float* tp = tile + (wid * 8 + i) * 257 + lane * 4; tp[0] = cur[i][0]; tp[1] = cur[i][1]; tp[2] = cur[i][2]; tp[3] = cur[i][3]; }
;         __syncthreads();
;         const int per = 16 * ntn, z = it / per, r = it % per, kt = r / ntn, nt = r % ntn;
;         bf16* d = dst + (size_t)z * N * 1024 + (((size_t)nt * 16 + kt) << 14);
;         const int kc = lane & 7;
; #pragma unroll
;         for (int pss = 0; pss < 4; ++pss) {
;             const int nn = wid * 32 + pss * 8 + (lane >> 3); float f[8];
; #pragma unroll
;             for (int j = 0; j < 8; ++j) f[j] = tile[(kc * 8 + j) * 257 + nn];
;             u32x4 w; w.x = g8_cvt_pk(f[0], f[1]); w.y = g8_cvt_pk(f[2], f[3]); w.z = g8_cvt_pk(f[4], f[5]); w.w = g8_cvt_pk(f[6], f[7]);
;             *(u32x4*)(d + nn * 64 + kc * 8) = w;
;         }
.LBB0_1616:
	s_or_b64 exec, exec, s[4:5]
	s_waitcnt lgkmcnt(0)
	s_barrier
	ds_read_b32 v11, v15
	s_mov_b64 s[4:5], -1
	s_waitcnt lgkmcnt(0)
	v_cmp_lt_i32_e32 vcc, s11, v11
	v_readfirstlane_b32 s0, v11
	s_cbranch_vccnz .LBB0_1611
	s_cmpk_gt_i32 s0, 0xfff
	s_cselect_b64 vcc, -1, 0
	s_and_b64 s[4:5], vcc, exec
	s_cselect_b32 s4, s13, 0x104e000
	s_cselect_b32 s9, 0x400, s12
	s_cselect_b32 s15, s73, s69
	s_cselect_b32 s18, s72, s68
	s_cselect_b32 s5, s14, 0x1000
	s_cselect_b32 s16, 20, 21
	s_cselect_b32 s19, 10, 11
	s_add_u32 s20, s78, s4
	s_addc_u32 s21, s79, 0
	s_lshr_b32 s6, s9, 4
	s_abs_i32 s4, s6
	v_cvt_f32_u32_e32 v11, s4
	s_sub_i32 s17, 0, s4
	s_add_i32 s5, s5, s0
	s_abs_i32 s7, s5
	v_rcp_iflag_f32_e32 v11, v11
	s_xor_b32 s0, s5, s6
	s_lshr_b32 s8, s9, 8
	s_ashr_i32 s0, s0, 31
	v_mul_f32_e32 v11, 0x4f7ffffe, v11
	v_cvt_u32_f32_e32 v11, v11
	s_nop 0
	v_readfirstlane_b32 s22, v11
	s_mul_i32 s17, s17, s22
	s_mul_hi_u32 s17, s22, s17
	s_add_i32 s22, s22, s17
	s_mul_hi_u32 s17, s7, s22
	s_mul_i32 s22, s17, s4
	s_sub_i32 s7, s7, s22
	s_add_i32 s22, s17, 1
	s_sub_i32 s23, s7, s4
	s_cmp_ge_u32 s7, s4
	s_cselect_b32 s17, s22, s17
	s_cselect_b32 s7, s23, s7
	s_add_i32 s22, s17, 1
	s_cmp_ge_u32 s7, s4
	s_cselect_b32 s4, s22, s17
	s_xor_b32 s4, s4, s0
	s_sub_i32 s4, s4, s0
	s_sext_i32_i8 s0, s8
	v_cvt_f32_i32_e32 v11, s0
	s_mul_i32 s6, s4, s6
	s_sub_i32 s5, s5, s6
	v_cvt_f32_i32_e32 v28, s5
	v_rcp_iflag_f32_e32 v29, v11
	s_xor_b32 s0, s5, s0
	s_ashr_i32 s0, s0, 30
	s_or_b32 s0, s0, 1
	v_mul_f32_e32 v29, v28, v29
	v_trunc_f32_e32 v29, v29
	v_fma_f32 v28, -v29, v11, v28
	v_cvt_i32_f32_e32 v29, v29
	v_cmp_ge_f32_e64 s[6:7], |v28|, |v11|
	s_and_b64 s[6:7], s[6:7], exec
	s_cselect_b32 s0, s0, 0
	v_readfirstlane_b32 s6, v29
	s_add_i32 s6, s6, s0
	s_mul_i32 s7, s6, s8
	s_sub_i32 s8, s5, s7
	s_sext_i32_i8 s5, s8
	v_lshl_add_u32 v11, s5, 7, v12
	v_lshl_or_b32 v28, s5, 8, v13
	s_ashr_i32 s5, s4, 31
	s_sext_i32_i8 s0, s6
	s_lshl_b64 s[16:17], s[4:5], s16
	v_lshl_or_b32 v30, s0, 6, v14
	s_lshl_b64 s[16:17], s[16:17], 2
	v_ashrrev_i32_e32 v31, 31, v30
	s_add_u32 s16, s18, s16
	v_cndmask_b32_e32 v28, v11, v28, vcc
	s_addc_u32 s17, s15, s17
	v_lshlrev_b64 v[30:31], s19, v[30:31]
	v_lshl_add_u64 v[30:31], v[30:31], 2, s[16:17]
	v_ashrrev_i32_e32 v29, 31, v28
	v_lshl_add_u64 v[52:53], v[28:29], 2, v[30:31]
	s_lshl_b64 s[16:17], 12, s19
	s_lshl_b32 s0, s9, 2
	v_lshl_add_u64 v[40:41], v[52:53], 0, s[16:17]
	s_lshl_b64 s[16:17], 24, s19
	v_lshl_add_u64 v[36:37], v[52:53], 0, s[0:1]
	v_lshl_add_u64 v[44:45], v[52:53], 0, s[16:17]
	s_lshl_b64 s[16:17], 28, s19
	v_lshl_add_u64 v[54:55], v[36:37], 0, s[0:1]
	v_lshl_add_u64 v[48:49], v[52:53], 0, s[16:17]
	s_lshl_b32 s0, s9, 3
	s_lshl_b64 s[16:17], 20, s19
	global_load_dwordx4 v[28:31], v[52:53], off nt
	global_load_dwordx4 v[32:35], v[36:37], off nt
	s_nop 0
	global_load_dwordx4 v[36:39], v[54:55], off nt
	s_nop 0
	global_load_dwordx4 v[40:43], v[40:41], off nt
	v_lshl_add_u64 v[54:55], v[54:55], 0, s[0:1]
	v_lshl_add_u64 v[56:57], v[52:53], 0, s[16:17]
	global_load_dwordx4 v[44:47], v[44:45], off nt
	s_nop 0
	global_load_dwordx4 v[48:51], v[48:49], off nt
	s_nop 0
	global_load_dwordx4 v[52:55], v[54:55], off nt
	s_nop 0
	global_load_dwordx4 v[56:59], v[56:57], off nt
	s_lshl_b64 s[4:5], s[4:5], s19
	s_lshl_b64 s[4:5], s[4:5], 11
	s_add_u32 s0, s20, s4
	s_addc_u32 s9, s21, s5
	s_bfe_i64 s[4:5], s[8:9], 0x80000
	s_bfe_i64 s[6:7], s[6:7], 0x80000
	s_lshl_b64 s[4:5], s[4:5], 19
	s_add_u32 s0, s0, s4
	s_addc_u32 s8, s9, s5
	s_lshl_b64 s[4:5], s[6:7], 15
	s_add_u32 s4, s0, s4
	s_addc_u32 s5, s8, s5
	v_mov_b32_e32 v11, v3
	s_add_i32 s3, s3, -1
	s_cmp_eq_u32 s3, 0
	s_waitcnt vmcnt(7)
	ds_write_b128 v16, v[28:31]
	s_waitcnt vmcnt(6)
	ds_write2_b32 v17, v32, v33 offset1:1
	ds_write2_b32 v18, v34, v35 offset1:1
	s_waitcnt vmcnt(3)
	ds_write2_b64 v24, v[44:45], v[46:47] offset1:1
	s_waitcnt vmcnt(2)
	ds_write2_b32 v25, v48, v49 offset1:1
	ds_write2_b32 v26, v50, v51 offset1:1
	ds_write2_b64 v19, v[36:37], v[38:39] offset1:1
	ds_write2_b32 v20, v40, v41 offset1:1
	ds_write2_b32 v21, v42, v43 offset1:1
	s_waitcnt vmcnt(1)
	ds_write_b128 v16, v[52:55] offset:4112
	s_waitcnt vmcnt(0)
	ds_write2_b32 v22, v56, v57 offset1:1
	ds_write2_b32 v23, v58, v59 offset1:1
	s_waitcnt lgkmcnt(0)
	s_barrier
	ds_read_b32 v28, v27 offset:1028
	ds_read_b32 v29, v27 offset:3084
	ds_read_b32 v30, v27 offset:5140
	ds_read_b32 v31, v27 offset:7196
	ds_read_b32 v32, v27 offset:6168
	ds_read_b32 v33, v27 offset:4112
	ds_read_b32 v34, v27 offset:2056
	ds_read_b32 v35, v27
	s_waitcnt lgkmcnt(0)
	v_cvt_pk_bf16_f32 v28, v35, v28
	v_cvt_pk_bf16_f32 v29, v34, v29
	v_cvt_pk_bf16_f32 v30, v33, v30
	v_cvt_pk_bf16_f32 v31, v32, v31
	ds_read_b32 v36, v27 offset:1060
	ds_read_b32 v37, v27 offset:3116
	ds_read_b32 v38, v27 offset:5172
	ds_read_b32 v39, v27 offset:7228
	ds_read_b32 v40, v27 offset:6200
	ds_read_b32 v41, v27 offset:4144
	ds_read_b32 v42, v27 offset:2088
	ds_read_b32 v43, v27 offset:32
	v_lshl_add_u64 v[32:33], s[4:5], 0, v[2:3]
	v_lshl_add_u64 v[34:35], v[32:33], 0, v[10:11]
	global_store_dwordx4 v[34:35], v[28:31], off
	v_lshl_add_u64 v[34:35], v[4:5], 1, v[32:33]
	s_cselect_b64 s[4:5], -1, 0
	s_waitcnt lgkmcnt(0)
	v_cvt_pk_bf16_f32 v28, v43, v36
	v_cvt_pk_bf16_f32 v29, v42, v37
	v_cvt_pk_bf16_f32 v30, v41, v38
	v_cvt_pk_bf16_f32 v31, v40, v39
	ds_read_b32 v11, v27 offset:1092
	ds_read_b32 v36, v27 offset:3148
	ds_read_b32 v37, v27 offset:6232
	ds_read_b32 v38, v27 offset:4176
	ds_read_b32 v39, v27 offset:2120
	ds_read_b32 v40, v27 offset:64
	ds_read_b32 v41, v27 offset:5204
	ds_read_b32 v42, v27 offset:7260
	global_store_dwordx4 v[34:35], v[28:31], off
	v_lshl_add_u64 v[34:35], v[6:7], 1, v[32:33]
	v_lshl_add_u64 v[32:33], v[8:9], 1, v[32:33]
	s_waitcnt lgkmcnt(2)
	v_cvt_pk_bf16_f32 v28, v40, v11
	v_cvt_pk_bf16_f32 v29, v39, v36
	s_waitcnt lgkmcnt(1)
	v_cvt_pk_bf16_f32 v30, v38, v41
	s_waitcnt lgkmcnt(0)
	v_cvt_pk_bf16_f32 v31, v37, v42
	ds_read_b32 v11, v27 offset:1124
	ds_read_b32 v36, v27 offset:3180
	ds_read_b32 v37, v27 offset:6264
	ds_read_b32 v38, v27 offset:4208
	ds_read_b32 v39, v27 offset:2152
	ds_read_b32 v40, v27 offset:96
	ds_read_b32 v41, v27 offset:5236
	ds_read_b32 v42, v27 offset:7292
	global_store_dwordx4 v[34:35], v[28:31], off
	s_waitcnt lgkmcnt(2)
	s_nop 0
	v_cvt_pk_bf16_f32 v28, v40, v11
	v_cvt_pk_bf16_f32 v29, v39, v36
	s_waitcnt lgkmcnt(1)
	v_cvt_pk_bf16_f32 v30, v38, v41
	s_waitcnt lgkmcnt(0)
	v_cvt_pk_bf16_f32 v31, v37, v42
	global_store_dwordx4 v[32:33], v[28:31], off
	s_branch .LBB0_1611

; #define SEAM(k) do { if (IN(k) && IN((k) + 1)) xcd_barrier(bar); \
;         if (PROBE_MASK) { const unsigned long long t_ = __builtin_amdgcn_s_memrealtime(); if ((PROBE_MASK >> (k)) & 1u) pr_acc += t_ - pr_t0; pr_t0 = t_; } } while (0)
; __device__ __forceinline__ void convert_deferred(const Ptrs& P, unsigned char* lds, int quota) {
;     const int tid = threadIdx.x, wid = tid >> 6, lane = tid & 63;
;     float* tile = (float*)lds;
;     volatile __attribute__((address_space(3))) int* slot = (volatile __attribute__((address_space(3))) int*)((__attribute__((address_space(3))) unsigned char*)lds + 131072 + 320 + 11000);
;     unsigned* q = (unsigned*)(P.ws + WS_CTL) + CW_DEFQ;
;     for (int n = 0; n < quota; ++n) {
;         __syncthreads();
;         if (tid == 0) *slot = (int)atomicAdd(q, 1u);
;         __syncthreads();
;         const int t = *slot;
;         if (t >= DEF_GU + DEF_DN) break;
;         const bool gu = t < DEF_GU;
;         const float* src = gu ? P.in[34] : P.in[36]; bf16* dst = (bf16*)(P.ws + (gu ? WS_WGU : WS_WDN));
;         const int N = gu ? 2048 : 1024, ntn = N / 256, it = gu ? 2 * NE * 16 * 8 - DEF_GU + t : 2 * NE * 16 * 4 - DEF_DN + (t - DEF_GU);
; __global__ void __launch_bounds__(NT, 2) mega(Args args) {
;     ...
;         if (IDLE_LAST(68 * 12)) convert_deferred(P, lds, 4); } SEAM(11);
.LBB0_1851:
	s_abs_i32 s0, s62
	v_cvt_f32_u32_e32 v2, s0
	s_sub_i32 s3, 0, s0
	v_readlane_b32 s56, v254, 40
	s_mov_b32 s1, 0
	v_rcp_iflag_f32_e32 v2, v2
	v_readlane_b32 s57, v254, 41
	v_mul_f32_e32 v2, 0x4f7ffffe, v2
	v_cvt_u32_f32_e32 v2, v2
	s_nop 0
	v_readfirstlane_b32 s4, v2
	s_mul_i32 s3, s3, s4
	s_mul_hi_u32 s3, s4, s3
	s_add_i32 s4, s4, s3
	s_mul_hi_u32 s3, s4, 0x330
	s_mul_i32 s3, s3, s0
	s_sub_i32 s3, 0x330, s3
	s_sub_i32 s4, s3, s0
	s_cmp_ge_u32 s3, s0
	s_cselect_b32 s3, s4, s3
	s_sub_i32 s4, s3, s0
	s_cmp_ge_u32 s3, s0
	s_cselect_b32 s0, s4, s3
	s_cmp_eq_u32 s0, 0
	s_cselect_b64 s[4:5], -1, 0
	s_cmp_lt_i32 s2, s0
	s_cselect_b64 s[6:7], -1, 0
	s_or_b64 s[4:5], s[4:5], s[6:7]
	s_and_b64 vcc, exec, s[4:5]
	s_cbranch_vccnz .LBB0_1861
	v_and_b32_e32 v2, 0x7c, v218
	v_lshlrev_b32_e32 v3, 5, v0
	s_movk_i32 s0, 0x400
	v_and_or_b32 v12, v3, s0, v2
	v_bfe_u32 v2, v0, 3, 3
	v_lshl_or_b32 v4, v1, 5, v2
	v_lshlrev_b32_e32 v2, 3, v0
	v_lshl_add_u32 v11, v182, 4, 0
	v_and_b32_e32 v2, 56, v2
	v_mul_u32_u24_e32 v16, 0x2020, v1
	v_mov_b32_e32 v3, 0
	s_waitcnt vmcnt(0)
	v_lshl_add_u32 v27, v4, 2, 0
	v_mul_u32_u24_e32 v28, 0x404, v2
	v_lshlrev_b32_e32 v10, 6, v4
	s_add_i32 s10, 0, 0x22c38
	v_add_u32_e32 v16, v11, v16
	v_and_b32_e32 v13, 0xfc, v218
	v_and_b32_e32 v14, 56, v179
	s_mov_b32 s3, 12
	v_or_b32_e32 v4, 0x200, v10
	v_mov_b32_e32 v5, v3
	v_or_b32_e32 v6, 0x400, v10
	v_mov_b32_e32 v7, v3
	v_or_b32_e32 v8, 0x600, v10
	v_mov_b32_e32 v9, v3
	v_mov_b32_e32 v15, s10
	s_movk_i32 s11, 0x17ff
	s_movk_i32 s12, 0x800
	s_mov_b32 s13, 0x1104e000
	s_movk_i32 s14, -2048
	v_add_u32_e32 v17, 0x404, v16
	v_add_u32_e32 v18, 0x40c, v16
	v_add_u32_e32 v19, 0x808, v16
	v_add_u32_e32 v20, 0xc0c, v16
	v_add_u32_e32 v21, 0xc14, v16
	v_add_u32_e32 v22, 0x1414, v16
	v_add_u32_e32 v23, 0x141c, v16
	v_add_u32_e32 v24, 0x1818, v16
	v_add_u32_e32 v25, 0x1c1c, v16
	v_add_u32_e32 v26, 0x1c24, v16
	v_lshlrev_b32_e32 v2, 1, v2
	v_add_u32_e32 v27, v27, v28
	v_lshlrev_b32_e32 v10, 1, v10
	s_branch .LBB0_1854

; __device__ __forceinline__ unsigned g8_cvt_pk(float lo, float hi) { unsigned r; asm volatile("v_cvt_pk_bf16_f32 %0, %1, %2" : "=v"(r) : "v"(lo), "v"(hi)); return r; }
; __device__ __forceinline__ void bt_load(const float* __restrict__ src, int N, int perm, int it, int ntn, f32x4 (&v)[8]) {
;     const int wid = threadIdx.x >> 6, lane = threadIdx.x & 63;
;     const int per = 16 * ntn, z = it / per, r = it % per, kt = r / ntn, nt = r % ntn;
;     const int np = nt * 256 + lane * 4;
;     const int sc = perm ? (nt * 128 + (lane & 31) * 4 + (lane >> 5) * 1024) : np;
;     const float* p = src + (size_t)z * 1024 * N + (size_t)(kt * 64 + wid * 8) * N + sc;
; #pragma unroll
;     for (int i = 0; i < 8; ++i) v[i] = __builtin_nontemporal_load((const f32x4*)(p + (size_t)i * N));
; }
; __device__ __forceinline__ void convert_deferred(const Ptrs& P, unsigned char* lds, int quota) {
;     ...
;         __syncthreads();
;         if (tid == 0) *slot = (int)atomicAdd(q, 1u);
;         __syncthreads();
;         const int t = *slot;
;         if (t >= DEF_GU + DEF_DN) break;
;         const bool gu = t < DEF_GU;
;         const float* src = gu ? P.in[34] : P.in[36]; bf16* dst = (bf16*)(P.ws + (gu ? WS_WGU : WS_WDN));
;         const int N = gu ? 2048 : 1024, ntn = N / 256, it = gu ? 2 * NE * 16 * 8 - DEF_GU + t : 2 * NE * 16 * 4 - DEF_DN + (t - DEF_GU);
;         f32x4 cur[8];
;         bt_load(src, N, gu ? 1 : 0, it, ntn, cur);
; #pragma unroll
;         for (int i = 0; i < 8; ++i) { float* tp = tile + (wid * 8 + i) * 257 + lane * 4; tp[0] = cur[i][0]; tp[1] = cur[i][1]; tp[2] = cur[i][2]; tp[3] = cur[i][3]; }
;         __syncthreads();
;         const int per = 16 * ntn, z = it / per, r = it % per, kt = r / ntn, nt = r % ntn;
;         bf16* d = dst + (size_t)z * N * 1024 + (((size_t)nt * 16 + kt) << 14);
;         const int kc = lane & 7;
; #pragma unroll
;         for (int pss = 0; pss < 4; ++pss) {
;             const int nn = wid * 32 + pss * 8 + (lane >> 3); float f[8];
; #pragma unroll
;             for (int j = 0; j < 8; ++j) f[j] = tile[(kc * 8 + j) * 257 + nn];
;             u32x4 w; w.x = g8_cvt_pk(f[0], f[1]); w.y = g8_cvt_pk(f[2], f[3]); w.z = g8_cvt_pk(f[4], f[5]); w.w = g8_cvt_pk(f[6], f[7]);
;             *(u32x4*)(d + nn * 64 + kc * 8) = w;
;         }
.LBB0_1858:
	s_or_b64 exec, exec, s[4:5]
	s_waitcnt lgkmcnt(0)
	s_barrier
	ds_read_b32 v11, v15
	s_mov_b64 s[4:5], -1
	s_waitcnt lgkmcnt(0)
	v_cmp_lt_i32_e32 vcc, s11, v11
	v_readfirstlane_b32 s0, v11
	s_cbranch_vccnz .LBB0_1853
	s_cmpk_gt_i32 s0, 0xfff
	s_cselect_b64 vcc, -1, 0
	s_and_b64 s[4:5], vcc, exec
	s_cselect_b32 s4, s13, 0x104e000
	s_cselect_b32 s9, 0x400, s12
	s_cselect_b32 s15, s73, s69
	s_cselect_b32 s20, s72, s68
	s_cselect_b32 s5, s14, 0x1000
	s_cselect_b32 s16, 20, 21
	s_cselect_b32 s21, 10, 11
	s_add_u32 s22, s78, s4
	s_addc_u32 s23, s79, 0
	s_lshr_b32 s6, s9, 4
	s_abs_i32 s4, s6
	v_cvt_f32_u32_e32 v11, s4
	s_sub_i32 s17, 0, s4
	s_add_i32 s5, s5, s0
	s_abs_i32 s7, s5
	v_rcp_iflag_f32_e32 v11, v11
	s_xor_b32 s0, s5, s6
	s_lshr_b32 s8, s9, 8
	s_ashr_i32 s0, s0, 31
	v_mul_f32_e32 v11, 0x4f7ffffe, v11
	v_cvt_u32_f32_e32 v11, v11
	s_nop 0
	v_readfirstlane_b32 s24, v11
	s_mul_i32 s17, s17, s24
	s_mul_hi_u32 s17, s24, s17
	s_add_i32 s24, s24, s17
	s_mul_hi_u32 s17, s7, s24
	s_mul_i32 s24, s17, s4
	s_sub_i32 s7, s7, s24
	s_add_i32 s24, s17, 1
	s_sub_i32 s25, s7, s4
	s_cmp_ge_u32 s7, s4
	s_cselect_b32 s17, s24, s17
	s_cselect_b32 s7, s25, s7
	s_add_i32 s24, s17, 1
	s_cmp_ge_u32 s7, s4
	s_cselect_b32 s4, s24, s17
	s_xor_b32 s4, s4, s0
	s_sub_i32 s4, s4, s0
	s_sext_i32_i8 s0, s8
	v_cvt_f32_i32_e32 v11, s0
	s_mul_i32 s6, s4, s6
	s_sub_i32 s5, s5, s6
	v_cvt_f32_i32_e32 v28, s5
	v_rcp_iflag_f32_e32 v29, v11
	s_xor_b32 s0, s5, s0
	s_ashr_i32 s0, s0, 30
	s_or_b32 s0, s0, 1
	v_mul_f32_e32 v29, v28, v29
	v_trunc_f32_e32 v29, v29
	v_fma_f32 v28, -v29, v11, v28
	v_cvt_i32_f32_e32 v29, v29
	v_cmp_ge_f32_e64 s[6:7], |v28|, |v11|
	s_and_b64 s[6:7], s[6:7], exec
	s_cselect_b32 s0, s0, 0
	v_readfirstlane_b32 s6, v29
	s_add_i32 s6, s6, s0
	s_mul_i32 s7, s6, s8
	s_sub_i32 s8, s5, s7
	s_sext_i32_i8 s5, s8
	v_lshl_add_u32 v11, s5, 7, v12
	v_lshl_or_b32 v28, s5, 8, v13
	s_ashr_i32 s5, s4, 31
	s_sext_i32_i8 s0, s6
	s_lshl_b64 s[16:17], s[4:5], s16
	v_lshl_or_b32 v30, s0, 6, v14
	s_lshl_b64 s[16:17], s[16:17], 2
	v_ashrrev_i32_e32 v31, 31, v30
	s_add_u32 s16, s20, s16
	v_cndmask_b32_e32 v28, v11, v28, vcc
	s_addc_u32 s17, s15, s17
	v_lshlrev_b64 v[30:31], s21, v[30:31]
	v_lshl_add_u64 v[30:31], v[30:31], 2, s[16:17]
	v_ashrrev_i32_e32 v29, 31, v28
	v_lshl_add_u64 v[52:53], v[28:29], 2, v[30:31]
	s_lshl_b64 s[16:17], 12, s21
	s_lshl_b32 s0, s9, 2
	v_lshl_add_u64 v[40:41], v[52:53], 0, s[16:17]
	s_lshl_b64 s[16:17], 24, s21
	v_lshl_add_u64 v[36:37], v[52:53], 0, s[0:1]
	v_lshl_add_u64 v[44:45], v[52:53], 0, s[16:17]
	s_lshl_b64 s[16:17], 28, s21
	v_lshl_add_u64 v[54:55], v[36:37], 0, s[0:1]
	v_lshl_add_u64 v[48:49], v[52:53], 0, s[16:17]
	s_lshl_b32 s0, s9, 3
	s_lshl_b64 s[16:17], 20, s21
	global_load_dwordx4 v[28:31], v[52:53], off nt
	global_load_dwordx4 v[32:35], v[36:37], off nt
	s_nop 0
	global_load_dwordx4 v[36:39], v[54:55], off nt
	s_nop 0
	global_load_dwordx4 v[40:43], v[40:41], off nt
	v_lshl_add_u64 v[54:55], v[54:55], 0, s[0:1]
	v_lshl_add_u64 v[56:57], v[52:53], 0, s[16:17]
	global_load_dwordx4 v[44:47], v[44:45], off nt
	s_nop 0
	global_load_dwordx4 v[48:51], v[48:49], off nt
	s_nop 0
	global_load_dwordx4 v[52:55], v[54:55], off nt
	s_nop 0
	global_load_dwordx4 v[56:59], v[56:57], off nt
	s_lshl_b64 s[4:5], s[4:5], s21
	s_lshl_b64 s[4:5], s[4:5], 11
	s_add_u32 s0, s22, s4
	s_addc_u32 s9, s23, s5
	s_bfe_i64 s[4:5], s[8:9], 0x80000
	s_bfe_i64 s[6:7], s[6:7], 0x80000
	s_lshl_b64 s[4:5], s[4:5], 19
	s_add_u32 s0, s0, s4
	s_addc_u32 s8, s9, s5
	s_lshl_b64 s[4:5], s[6:7], 15
	s_add_u32 s4, s0, s4
	s_addc_u32 s5, s8, s5
	v_mov_b32_e32 v11, v3
	s_add_i32 s3, s3, -1
	s_cmp_eq_u32 s3, 0
	s_waitcnt vmcnt(7)
	ds_write_b128 v16, v[28:31]
	s_waitcnt vmcnt(6)
	ds_write2_b32 v17, v32, v33 offset1:1
	ds_write2_b32 v18, v34, v35 offset1:1
	s_waitcnt vmcnt(3)
	ds_write2_b64 v24, v[44:45], v[46:47] offset1:1
	s_waitcnt vmcnt(2)
	ds_write2_b32 v25, v48, v49 offset1:1
	ds_write2_b32 v26, v50, v51 offset1:1
	ds_write2_b64 v19, v[36:37], v[38:39] offset1:1
	ds_write2_b32 v20, v40, v41 offset1:1
	ds_write2_b32 v21, v42, v43 offset1:1
	s_waitcnt vmcnt(1)
	ds_write_b128 v16, v[52:55] offset:4112
	s_waitcnt vmcnt(0)
	ds_write2_b32 v22, v56, v57 offset1:1
	ds_write2_b32 v23, v58, v59 offset1:1
	s_waitcnt lgkmcnt(0)
	s_barrier
	ds_read_b32 v28, v27 offset:1028
	ds_read_b32 v29, v27 offset:3084
	ds_read_b32 v30, v27 offset:5140
	ds_read_b32 v31, v27 offset:7196
	ds_read_b32 v32, v27 offset:6168
	ds_read_b32 v33, v27 offset:4112
	ds_read_b32 v34, v27 offset:2056
	ds_read_b32 v35, v27
	s_waitcnt lgkmcnt(0)
	v_cvt_pk_bf16_f32 v28, v35, v28
	v_cvt_pk_bf16_f32 v29, v34, v29
	v_cvt_pk_bf16_f32 v30, v33, v30
	v_cvt_pk_bf16_f32 v31, v32, v31
	ds_read_b32 v36, v27 offset:1060
	ds_read_b32 v37, v27 offset:3116
	ds_read_b32 v38, v27 offset:5172
	ds_read_b32 v39, v27 offset:7228
	ds_read_b32 v40, v27 offset:6200
	ds_read_b32 v41, v27 offset:4144
	ds_read_b32 v42, v27 offset:2088
	ds_read_b32 v43, v27 offset:32
	v_lshl_add_u64 v[32:33], s[4:5], 0, v[2:3]
	v_lshl_add_u64 v[34:35], v[32:33], 0, v[10:11]
	global_store_dwordx4 v[34:35], v[28:31], off
	v_lshl_add_u64 v[34:35], v[4:5], 1, v[32:33]
	s_cselect_b64 s[4:5], -1, 0
	s_waitcnt lgkmcnt(0)
	v_cvt_pk_bf16_f32 v28, v43, v36
	v_cvt_pk_bf16_f32 v29, v42, v37
	v_cvt_pk_bf16_f32 v30, v41, v38
	v_cvt_pk_bf16_f32 v31, v40, v39
	ds_read_b32 v11, v27 offset:1092
	ds_read_b32 v36, v27 offset:3148
	ds_read_b32 v37, v27 offset:6232
	ds_read_b32 v38, v27 offset:4176
	ds_read_b32 v39, v27 offset:2120
	ds_read_b32 v40, v27 offset:64
	ds_read_b32 v41, v27 offset:5204
	ds_read_b32 v42, v27 offset:7260
	global_store_dwordx4 v[34:35], v[28:31], off
	v_lshl_add_u64 v[34:35], v[6:7], 1, v[32:33]
	v_lshl_add_u64 v[32:33], v[8:9], 1, v[32:33]
	s_waitcnt lgkmcnt(2)
	v_cvt_pk_bf16_f32 v28, v40, v11
	v_cvt_pk_bf16_f32 v29, v39, v36
	s_waitcnt lgkmcnt(1)
	v_cvt_pk_bf16_f32 v30, v38, v41
	s_waitcnt lgkmcnt(0)
	v_cvt_pk_bf16_f32 v31, v37, v42
	ds_read_b32 v11, v27 offset:1124
	ds_read_b32 v36, v27 offset:3180
	ds_read_b32 v37, v27 offset:6264
	ds_read_b32 v38, v27 offset:4208
	ds_read_b32 v39, v27 offset:2152
	ds_read_b32 v40, v27 offset:96
	ds_read_b32 v41, v27 offset:5236
	ds_read_b32 v42, v27 offset:7292
	global_store_dwordx4 v[34:35], v[28:31], off
	s_waitcnt lgkmcnt(2)
	s_nop 0
	v_cvt_pk_bf16_f32 v28, v40, v11
	v_cvt_pk_bf16_f32 v29, v39, v36
	s_waitcnt lgkmcnt(1)
	v_cvt_pk_bf16_f32 v30, v38, v41
	s_waitcnt lgkmcnt(0)
	v_cvt_pk_bf16_f32 v31, v37, v42
	global_store_dwordx4 v[32:33], v[28:31], off
	s_branch .LBB0_1853

; #define SEAM(k) do { if (IN(k) && IN((k) + 1)) xcd_barrier(bar); \
;         if (PROBE_MASK) { const unsigned long long t_ = __builtin_amdgcn_s_memrealtime(); if ((PROBE_MASK >> (k)) & 1u) pr_acc += t_ - pr_t0; pr_t0 = t_; } } while (0)
; __device__ __forceinline__ void convert_deferred(const Ptrs& P, unsigned char* lds, int quota) {
;     const int tid = threadIdx.x, wid = tid >> 6, lane = tid & 63;
;     float* tile = (float*)lds;
;     volatile __attribute__((address_space(3))) int* slot = (volatile __attribute__((address_space(3))) int*)((__attribute__((address_space(3))) unsigned char*)lds + 131072 + 320 + 11000);
;     unsigned* q = (unsigned*)(P.ws + WS_CTL) + CW_DEFQ;
;     for (int n = 0; n < quota; ++n) {
;         __syncthreads();
;         if (tid == 0) *slot = (int)atomicAdd(q, 1u);
;         __syncthreads();
;         const int t = *slot;
;         if (t >= DEF_GU + DEF_DN) break;
;         const bool gu = t < DEF_GU;
;         const float* src = gu ? P.in[34] : P.in[36]; bf16* dst = (bf16*)(P.ws + (gu ? WS_WGU : WS_WDN));
;         const int N = gu ? 2048 : 1024, ntn = N / 256, it = gu ? 2 * NE * 16 * 8 - DEF_GU + t : 2 * NE * 16 * 4 - DEF_DN + (t - DEF_GU);
; __global__ void __launch_bounds__(NT, 2) mega(Args args) {
;     ...
;     if (IN(15)) { ph_norm2_router(P, lds, 1, 1); convert_deferred(P, lds, 1 << 20); } SEAM(15);
.LBB0_2278:
	v_and_b32_e32 v2, 0x7c, v179
	v_lshlrev_b32_e32 v3, 5, v0
	s_movk_i32 s0, 0x400
	v_and_or_b32 v12, v3, s0, v2
	v_lshrrev_b32_e32 v2, 3, v0
	v_and_b32_e32 v14, 56, v2
	v_lshrrev_b32_e32 v2, 3, v182
	v_lshl_or_b32 v4, v1, 5, v2
	v_lshl_add_u32 v5, v182, 4, 0
	v_and_b32_e32 v2, 56, v188
	v_lshl_add_u32 v7, v4, 2, 0
	v_mul_u32_u24_e32 v11, 0x2020, v1
	v_lshlrev_b32_e32 v4, 6, v4
	v_mul_u32_u24_e32 v9, 0x404, v2
	v_or_b32_e32 v6, 0x200, v4
	v_or_b32_e32 v8, 0x400, v4
	v_or_b32_e32 v10, 0x600, v4
	s_add_i32 s10, 0, 0x22c38
	v_add_u32_e32 v16, v5, v11
	v_and_b32_e32 v13, 0xfc, v179
	s_mov_b32 s1, 0
	v_mov_b32_e32 v3, 0
	s_mov_b32 s3, 0x100000
	v_mov_b32_e32 v15, s10
	s_movk_i32 s11, 0x17ff
	s_movk_i32 s12, 0x800
	s_mov_b32 s13, 0x1104e000
	s_movk_i32 s14, -2048
	v_add_u32_e32 v17, 0x404, v16
	v_add_u32_e32 v18, 0x40c, v16
	v_add_u32_e32 v19, 0x808, v16
	v_add_u32_e32 v20, 0xc0c, v16
	v_add_u32_e32 v21, 0xc14, v16
	v_add_u32_e32 v22, 0x1414, v16
	v_add_u32_e32 v23, 0x141c, v16
	v_add_u32_e32 v24, 0x1818, v16
	v_add_u32_e32 v25, 0x1c1c, v16
	v_add_u32_e32 v26, 0x1c24, v16
	v_lshlrev_b32_e32 v2, 1, v2
	v_add_u32_e32 v27, v7, v9
	v_lshlrev_b32_e32 v4, 1, v4
	v_lshlrev_b32_e32 v6, 1, v6
	v_lshlrev_b32_e32 v8, 1, v8
	v_lshlrev_b32_e32 v10, 1, v10
	s_branch .LBB0_2280

; __device__ __forceinline__ unsigned g8_cvt_pk(float lo, float hi) { unsigned r; asm volatile("v_cvt_pk_bf16_f32 %0, %1, %2" : "=v"(r) : "v"(lo), "v"(hi)); return r; }
; __device__ __forceinline__ void bt_load(const float* __restrict__ src, int N, int perm, int it, int ntn, f32x4 (&v)[8]) {
;     const int wid = threadIdx.x >> 6, lane = threadIdx.x & 63;
;     const int per = 16 * ntn, z = it / per, r = it % per, kt = r / ntn, nt = r % ntn;
;     const int np = nt * 256 + lane * 4;
;     const int sc = perm ? (nt * 128 + (lane & 31) * 4 + (lane >> 5) * 1024) : np;
;     const float* p = src + (size_t)z * 1024 * N + (size_t)(kt * 64 + wid * 8) * N + sc;
; #pragma unroll
;     for (int i = 0; i < 8; ++i) v[i] = __builtin_nontemporal_load((const f32x4*)(p + (size_t)i * N));
; }
; __device__ __forceinline__ void convert_deferred(const Ptrs& P, unsigned char* lds, int quota) {
;     ...
;         __syncthreads();
;         if (tid == 0) *slot = (int)atomicAdd(q, 1u);
;         __syncthreads();
;         const int t = *slot;
;         if (t >= DEF_GU + DEF_DN) break;
;         const bool gu = t < DEF_GU;
;         const float* src = gu ? P.in[34] : P.in[36]; bf16* dst = (bf16*)(P.ws + (gu ? WS_WGU : WS_WDN));
;         const int N = gu ? 2048 : 1024, ntn = N / 256, it = gu ? 2 * NE * 16 * 8 - DEF_GU + t : 2 * NE * 16 * 4 - DEF_DN + (t - DEF_GU);
;         f32x4 cur[8];
;         bt_load(src, N, gu ? 1 : 0, it, ntn, cur);
; #pragma unroll
;         for (int i = 0; i < 8; ++i) { float* tp = tile + (wid * 8 + i) * 257 + lane * 4; tp[0] = cur[i][0]; tp[1] = cur[i][1]; tp[2] = cur[i][2]; tp[3] = cur[i][3]; }
;         __syncthreads();
;         const int per = 16 * ntn, z = it / per, r = it % per, kt = r / ntn, nt = r % ntn;
;         bf16* d = dst + (size_t)z * N * 1024 + (((size_t)nt * 16 + kt) << 14);
;         const int kc = lane & 7;
; #pragma unroll
;         for (int pss = 0; pss < 4; ++pss) {
;             const int nn = wid * 32 + pss * 8 + (lane >> 3); float f[8];
; #pragma unroll
;             for (int j = 0; j < 8; ++j) f[j] = tile[(kc * 8 + j) * 257 + nn];
;             u32x4 w; w.x = g8_cvt_pk(f[0], f[1]); w.y = g8_cvt_pk(f[2], f[3]); w.z = g8_cvt_pk(f[4], f[5]); w.w = g8_cvt_pk(f[6], f[7]);
;             *(u32x4*)(d + nn * 64 + kc * 8) = w;
;         }
.LBB0_2284:
	s_or_b64 exec, exec, s[4:5]
	s_waitcnt lgkmcnt(0)
	s_barrier
	ds_read_b32 v5, v15
	s_mov_b64 s[4:5], -1
	s_waitcnt lgkmcnt(0)
	v_cmp_lt_i32_e32 vcc, s11, v5
	v_readfirstlane_b32 s0, v5
	s_cbranch_vccnz .LBB0_2279
	s_cmpk_gt_i32 s0, 0xfff
	s_cselect_b64 vcc, -1, 0
	s_and_b64 s[4:5], vcc, exec
	s_cselect_b32 s4, s13, 0x104e000
	s_cselect_b32 s9, 0x400, s12
	s_cselect_b32 s15, s73, s69
	s_cselect_b32 s18, s72, s68
	s_cselect_b32 s5, s14, 0x1000
	s_cselect_b32 s16, 20, 21
	s_cselect_b32 s19, 10, 11
	s_add_u32 s22, s78, s4
	s_addc_u32 s23, s79, 0
	s_lshr_b32 s6, s9, 4
	s_abs_i32 s4, s6
	v_cvt_f32_u32_e32 v5, s4
	s_sub_i32 s17, 0, s4
	s_add_i32 s5, s5, s0
	s_abs_i32 s7, s5
	v_rcp_iflag_f32_e32 v5, v5
	s_xor_b32 s0, s5, s6
	s_lshr_b32 s8, s9, 8
	s_ashr_i32 s0, s0, 31
	v_mul_f32_e32 v5, 0x4f7ffffe, v5
	v_cvt_u32_f32_e32 v5, v5
	s_nop 0
	v_readfirstlane_b32 s24, v5
	s_mul_i32 s17, s17, s24
	s_mul_hi_u32 s17, s24, s17
	s_add_i32 s24, s24, s17
	s_mul_hi_u32 s17, s7, s24
	s_mul_i32 s24, s17, s4
	s_sub_i32 s7, s7, s24
	s_add_i32 s24, s17, 1
	s_sub_i32 s25, s7, s4
	s_cmp_ge_u32 s7, s4
	s_cselect_b32 s17, s24, s17
	s_cselect_b32 s7, s25, s7
	s_add_i32 s24, s17, 1
	s_cmp_ge_u32 s7, s4
	s_cselect_b32 s4, s24, s17
	s_xor_b32 s4, s4, s0
	s_sub_i32 s4, s4, s0
	s_sext_i32_i8 s0, s8
	v_cvt_f32_i32_e32 v5, s0
	s_mul_i32 s6, s4, s6
	s_sub_i32 s5, s5, s6
	v_cvt_f32_i32_e32 v7, s5
	v_rcp_iflag_f32_e32 v9, v5
	s_xor_b32 s0, s5, s0
	s_ashr_i32 s0, s0, 30
	s_or_b32 s0, s0, 1
	v_mul_f32_e32 v9, v7, v9
	v_trunc_f32_e32 v9, v9
	v_fma_f32 v7, -v9, v5, v7
	v_cvt_i32_f32_e32 v9, v9
	v_cmp_ge_f32_e64 s[6:7], |v7|, |v5|
	s_and_b64 s[6:7], s[6:7], exec
	s_cselect_b32 s0, s0, 0
	v_readfirstlane_b32 s6, v9
	s_add_i32 s6, s6, s0
	s_mul_i32 s7, s6, s8
	s_sub_i32 s8, s5, s7
	s_sext_i32_i8 s5, s8
	v_lshl_add_u32 v5, s5, 7, v12
	v_lshl_or_b32 v7, s5, 8, v13
	s_ashr_i32 s5, s4, 31
	s_sext_i32_i8 s0, s6
	s_lshl_b64 s[16:17], s[4:5], s16
	v_lshl_or_b32 v30, s0, 6, v14
	s_lshl_b64 s[16:17], s[16:17], 2
	v_ashrrev_i32_e32 v31, 31, v30
	s_add_u32 s16, s18, s16
	v_cndmask_b32_e32 v28, v5, v7, vcc
	s_addc_u32 s17, s15, s17
	v_lshlrev_b64 v[30:31], s19, v[30:31]
	v_lshl_add_u64 v[30:31], v[30:31], 2, s[16:17]
	v_ashrrev_i32_e32 v29, 31, v28
	v_lshl_add_u64 v[52:53], v[28:29], 2, v[30:31]
	s_lshl_b32 s0, s9, 2
	s_lshl_b64 s[16:17], 12, s19
	v_lshl_add_u64 v[36:37], v[52:53], 0, s[0:1]
	v_lshl_add_u64 v[44:45], v[52:53], 0, s[16:17]
	s_lshl_b64 s[16:17], 24, s19
	v_lshl_add_u64 v[54:55], v[36:37], 0, s[0:1]
	v_lshl_add_u64 v[56:57], v[52:53], 0, s[16:17]
	s_lshl_b64 s[16:17], 28, s19
	s_lshl_b32 s0, s9, 3
	v_lshl_add_u64 v[58:59], v[52:53], 0, s[16:17]
	v_lshl_add_u64 v[60:61], v[54:55], 0, s[0:1]
	s_lshl_b64 s[16:17], 20, s19
	global_load_dwordx4 v[28:31], v[52:53], off nt
	global_load_dwordx4 v[32:35], v[36:37], off nt
	s_nop 0
	global_load_dwordx4 v[36:39], v[54:55], off nt
	global_load_dwordx4 v[40:43], v[44:45], off nt
	s_nop 0
	global_load_dwordx4 v[44:47], v[56:57], off nt
	global_load_dwordx4 v[48:51], v[58:59], off nt
	v_lshl_add_u64 v[62:63], v[52:53], 0, s[16:17]
	global_load_dwordx4 v[52:55], v[60:61], off nt
	global_load_dwordx4 v[56:59], v[62:63], off nt
	s_lshl_b64 s[4:5], s[4:5], s19
	s_lshl_b64 s[4:5], s[4:5], 11
	s_add_u32 s0, s22, s4
	s_addc_u32 s9, s23, s5
	s_bfe_i64 s[4:5], s[8:9], 0x80000
	s_bfe_i64 s[6:7], s[6:7], 0x80000
	s_lshl_b64 s[4:5], s[4:5], 19
	s_add_u32 s0, s0, s4
	s_addc_u32 s8, s9, s5
	s_lshl_b64 s[4:5], s[6:7], 15
	s_add_u32 s4, s0, s4
	s_addc_u32 s5, s8, s5
	v_mov_b32_e32 v5, v3
	s_add_i32 s3, s3, -1
	s_cmp_eq_u32 s3, 0
	s_waitcnt vmcnt(7)
	ds_write_b128 v16, v[28:31]
	s_waitcnt vmcnt(6)
	ds_write2_b32 v17, v32, v33 offset1:1
	ds_write2_b32 v18, v34, v35 offset1:1
	s_waitcnt vmcnt(3)
	ds_write2_b64 v24, v[44:45], v[46:47] offset1:1
	s_waitcnt vmcnt(2)
	ds_write2_b32 v25, v48, v49 offset1:1
	ds_write2_b32 v26, v50, v51 offset1:1
	ds_write2_b64 v19, v[36:37], v[38:39] offset1:1
	ds_write2_b32 v20, v40, v41 offset1:1
	ds_write2_b32 v21, v42, v43 offset1:1
	s_waitcnt vmcnt(1)
	ds_write_b128 v16, v[52:55] offset:4112
	s_waitcnt vmcnt(0)
	ds_write2_b32 v22, v56, v57 offset1:1
	ds_write2_b32 v23, v58, v59 offset1:1
	s_waitcnt lgkmcnt(0)
	s_barrier
	ds_read_b32 v7, v27 offset:1028
	ds_read_b32 v9, v27 offset:3084
	ds_read_b32 v11, v27 offset:5140
	ds_read_b32 v31, v27 offset:7196
	ds_read_b32 v32, v27 offset:6168
	ds_read_b32 v30, v27 offset:4112
	ds_read_b32 v29, v27 offset:2056
	ds_read_b32 v28, v27
	s_waitcnt lgkmcnt(0)
	v_cvt_pk_bf16_f32 v28, v28, v7
	v_cvt_pk_bf16_f32 v29, v29, v9
	v_cvt_pk_bf16_f32 v30, v30, v11
	v_cvt_pk_bf16_f32 v31, v32, v31
	ds_read_b32 v7, v27 offset:1060
	ds_read_b32 v9, v27 offset:3116
	ds_read_b32 v11, v27 offset:5172
	ds_read_b32 v36, v27 offset:7228
	ds_read_b32 v37, v27 offset:6200
	ds_read_b32 v38, v27 offset:4144
	ds_read_b32 v39, v27 offset:2088
	ds_read_b32 v40, v27 offset:32
	v_lshl_add_u64 v[32:33], s[4:5], 0, v[2:3]
	v_lshl_add_u64 v[34:35], v[32:33], 0, v[4:5]
	global_store_dwordx4 v[34:35], v[28:31], off
	s_cselect_b64 s[4:5], -1, 0
	s_waitcnt lgkmcnt(0)
	v_cvt_pk_bf16_f32 v28, v40, v7
	v_cvt_pk_bf16_f32 v29, v39, v9
	v_cvt_pk_bf16_f32 v30, v38, v11
	v_cvt_pk_bf16_f32 v31, v37, v36
	ds_read_b32 v5, v27 offset:1092
	ds_read_b32 v9, v27 offset:3148
	ds_read_b32 v11, v27 offset:5204
	ds_read_b32 v36, v27 offset:6232
	ds_read_b32 v37, v27 offset:4176
	ds_read_b32 v38, v27 offset:2120
	ds_read_b32 v39, v27 offset:64
	ds_read_b32 v40, v27 offset:7260
	v_mov_b32_e32 v7, v3
	v_lshl_add_u64 v[34:35], v[32:33], 0, v[6:7]
	global_store_dwordx4 v[34:35], v[28:31], off
	s_waitcnt lgkmcnt(1)
	s_nop 0
	v_cvt_pk_bf16_f32 v28, v39, v5
	v_cvt_pk_bf16_f32 v29, v38, v9
	v_cvt_pk_bf16_f32 v30, v37, v11
	s_waitcnt lgkmcnt(0)
	v_cvt_pk_bf16_f32 v31, v36, v40
	ds_read_b32 v5, v27 offset:1124
	ds_read_b32 v7, v27 offset:3180
	ds_read_b32 v11, v27 offset:5236
	ds_read_b32 v36, v27 offset:6264
	ds_read_b32 v37, v27 offset:4208
	ds_read_b32 v38, v27 offset:2152
	ds_read_b32 v39, v27 offset:96
	ds_read_b32 v40, v27 offset:7292
	v_mov_b32_e32 v9, v3
	v_lshl_add_u64 v[34:35], v[32:33], 0, v[8:9]
	global_store_dwordx4 v[34:35], v[28:31], off
	s_waitcnt lgkmcnt(1)
	s_nop 0
	v_cvt_pk_bf16_f32 v28, v39, v5
	v_cvt_pk_bf16_f32 v29, v38, v7
	v_cvt_pk_bf16_f32 v30, v37, v11
	v_mov_b32_e32 v11, v3
	v_lshl_add_u64 v[32:33], v[32:33], 0, v[10:11]
	s_waitcnt lgkmcnt(0)
	v_cvt_pk_bf16_f32 v31, v36, v40
	global_store_dwordx4 v[32:33], v[28:31], off
	s_branch .LBB0_2279
